# speedup vs baseline: 1.0120x; 1.0034x over previous
.LBB2_24:
	s_or_b64 exec, exec, s[0:1]
	v_and_b32_e32 v1, 31, v0
	v_lshlrev_b32_e32 v2, 2, v1
	v_lshl_or_b32 v2, s10, 7, v2
	v_or_b32_e32 v2, 0x1ee00, v2
	v_lshrrev_b32_e32 v158, 5, v156
	s_waitcnt lgkmcnt(0)
	s_barrier
	v_lshlrev_b32_e32 v250, 4, v158
	v_lshl_or_b32 v250, s10, 7, v250
	v_or_b32_e32 v254, 0x1ee00, v250
	ds_read_b128 v[168:171], v254 offset:0
	ds_read_b128 v[172:175], v254 offset:32
	ds_read_b128 v[176:179], v254 offset:64
	ds_read_b128 v[180:183], v254 offset:96
	v_bfe_u32 v255, v156, 2, 2
	v_lshl_add_u32 v250, v255, 2, v250
	v_add_u32_e32 v250, 0x1e400, v250
	s_waitcnt lgkmcnt(0)
	s_barrier
	ds_read_b32 v157, v2
	v_mul_u32_u24_e32 v2, 0x88, v1
	s_mul_i32 s0, s11, 0x4400
	v_lshlrev_b32_e32 v2, 1, v2
	v_lshlrev_b32_e32 v3, 4, v158
	v_mov_b32_e32 v138, v0
	v_add3_u32 v159, s0, v2, v3
	ds_read_b128 v[2:5], v159
	ds_read_b128 v[18:21], v159 offset:8704
	ds_read_b128 v[130:133], v159 offset:32
	s_waitcnt vmcnt(10) lgkmcnt(2)
	v_mfma_f32_32x32x16_f16 v[50:65], v[2:5], v[126:129], 0
	s_mov_b32 s4, 0xc060c00
	s_mov_b32 s5, 0xe400
	s_mulk_i32 s11, 0x2400
	s_lshl_b32 s0, s10, 6
	s_or_b32 s0, s11, s0
	s_add_i32 s0, s0, 0x11000
	v_mul_u32_u24_e32 v251, 0x90, v1
	v_lshl_add_u32 v251, v158, 3, v251
	v_add_u32_e32 v251, s0, v251
	s_waitcnt lgkmcnt(1)
	v_mfma_f32_32x32x16_f16 v[34:49], v[18:21], v[126:129], 0
	s_or_b32 s0, s8, 2
	s_ashr_i32 s1, s0, 31
	s_lshl_b64 s[0:1], s[0:1], 12
	s_add_u32 s0, s2, s0
	s_addc_u32 s1, s3, s1
	v_cmp_gt_u32_e32 vcc, 32, v156
	v_mfma_f32_32x32x16_f16 v[2:17], v[122:125], v[2:5], v[168:183]
	v_mfma_f32_32x32x16_f16 v[18:33], v[122:125], v[18:21], v[168:183]
	ds_read_b128 v[134:137], v159 offset:8736
	ds_read_b128 v[160:163], v159 offset:64
	s_waitcnt vmcnt(8) lgkmcnt(2)
	v_mfma_f32_32x32x16_f16 v[50:65], v[130:133], v[118:121], v[50:65]
	s_waitcnt lgkmcnt(1)
	v_mfma_f32_32x32x16_f16 v[34:49], v[134:137], v[118:121], v[34:49]
	v_mfma_f32_32x32x16_f16 v[2:17], v[114:117], v[130:133], v[2:17]
	v_mfma_f32_32x32x16_f16 v[18:33], v[114:117], v[134:137], v[18:33]
	ds_read_b128 v[130:133], v159 offset:8768
	ds_read_b128 v[134:137], v159 offset:96
	s_waitcnt vmcnt(6) lgkmcnt(2)
	v_mfma_f32_32x32x16_f16 v[50:65], v[160:163], v[110:113], v[50:65]
	s_waitcnt lgkmcnt(1)
	v_mfma_f32_32x32x16_f16 v[34:49], v[130:133], v[110:113], v[34:49]
	v_mfma_f32_32x32x16_f16 v[2:17], v[106:109], v[160:163], v[2:17]
	v_mfma_f32_32x32x16_f16 v[18:33], v[106:109], v[130:133], v[18:33]
	ds_read_b128 v[130:133], v159 offset:8800
	ds_read_b128 v[160:163], v159 offset:128
	s_waitcnt vmcnt(4) lgkmcnt(2)
	v_mfma_f32_32x32x16_f16 v[50:65], v[134:137], v[102:105], v[50:65]
	s_waitcnt lgkmcnt(1)
	v_mfma_f32_32x32x16_f16 v[34:49], v[130:133], v[102:105], v[34:49]
	v_mfma_f32_32x32x16_f16 v[2:17], v[98:101], v[134:137], v[2:17]
	v_mfma_f32_32x32x16_f16 v[18:33], v[98:101], v[130:133], v[18:33]
	ds_read_b128 v[130:133], v159 offset:8832
	ds_read_b128 v[134:137], v159 offset:160
	s_waitcnt vmcnt(3) lgkmcnt(2)
	v_mfma_f32_32x32x16_f16 v[50:65], v[160:163], v[94:97], v[50:65]
	s_waitcnt lgkmcnt(1)
	v_mfma_f32_32x32x16_f16 v[34:49], v[130:133], v[94:97], v[34:49]
	v_mfma_f32_32x32x16_f16 v[2:17], v[86:89], v[160:163], v[2:17]
	v_mfma_f32_32x32x16_f16 v[18:33], v[86:89], v[130:133], v[18:33]
	ds_read_b128 v[130:133], v159 offset:8864
	ds_read_b128 v[160:163], v159 offset:192
	s_waitcnt vmcnt(2) lgkmcnt(2)
	v_mfma_f32_32x32x16_f16 v[50:65], v[134:137], v[90:93], v[50:65]
	s_waitcnt lgkmcnt(1)
	v_mfma_f32_32x32x16_f16 v[34:49], v[130:133], v[90:93], v[34:49]
	v_mfma_f32_32x32x16_f16 v[2:17], v[78:81], v[134:137], v[2:17]
	v_mfma_f32_32x32x16_f16 v[18:33], v[78:81], v[130:133], v[18:33]
	ds_read_b128 v[130:133], v159 offset:8896
	ds_read_b128 v[164:167], v159 offset:224
	s_waitcnt vmcnt(1) lgkmcnt(2)
	v_mfma_f32_32x32x16_f16 v[50:65], v[160:163], v[82:85], v[50:65]
	s_waitcnt lgkmcnt(1)
	v_mfma_f32_32x32x16_f16 v[34:49], v[130:133], v[82:85], v[34:49]
	v_mfma_f32_32x32x16_f16 v[2:17], v[70:73], v[160:163], v[2:17]
	v_mfma_f32_32x32x16_f16 v[18:33], v[70:73], v[130:133], v[18:33]
	v_lshlrev_b32_e32 v130, 3, v138
	v_and_b32_e32 v241, 0x1f8, v130
	global_load_dwordx2 v[138:139], v241, s[0:1]
	global_load_dwordx2 v[134:135], v241, s[0:1] offset:512
	global_load_dwordx2 v[132:133], v241, s[0:1] offset:1024
	global_load_dwordx2 v[130:131], v241, s[0:1] offset:1536
	global_load_dwordx2 v[136:137], v241, s[0:1] offset:2048
	s_waitcnt vmcnt(5) lgkmcnt(0)
	v_mfma_f32_32x32x16_f16 v[50:65], v[164:167], v[74:77], v[50:65]
	v_mfma_f32_32x32x16_f16 v[2:17], v[66:69], v[164:167], v[2:17]
	s_nop 10
	v_cvt_pk_f16_f32 v57, v56, v57
	v_cvt_pk_f16_f32 v56, v54, v55
	v_cvt_pk_f16_f32 v55, v52, v53
	v_cvt_pk_f16_f32 v54, v50, v51
	v_perm_b32 v50, v240, v154, s42
	v_perm_b32 v51, v240, v154, s43
	v_perm_b32 v52, v240, v155, s42
	v_perm_b32 v53, v240, v155, s43
	v_pk_add_f16 v50, v50, s5 op_sel_hi:[1,0]
	v_pk_add_f16 v51, v51, s5 op_sel_hi:[1,0]
	v_pk_add_f16 v52, v52, s5 op_sel_hi:[1,0]
	v_pk_add_f16 v53, v53, s5 op_sel_hi:[1,0]
	v_cvt_pk_f16_f32 v65, v64, v65
	v_cvt_pk_f16_f32 v64, v62, v63
	v_cvt_pk_f16_f32 v63, v60, v61
	v_cvt_pk_f16_f32 v62, v58, v59
	v_mfma_f32_32x32x16_f16 v[2:17], v[54:57], v[50:53], v[2:17]
	v_perm_b32 v58, v240, v150, s42
	v_perm_b32 v59, v240, v150, s43
	v_perm_b32 v60, v240, v151, s42
	v_perm_b32 v61, v240, v151, s43
	v_pk_add_f16 v58, v58, s5 op_sel_hi:[1,0]
	v_pk_add_f16 v59, v59, s5 op_sel_hi:[1,0]
	v_pk_add_f16 v60, v60, s5 op_sel_hi:[1,0]
	v_pk_add_f16 v61, v61, s5 op_sel_hi:[1,0]
	s_nop 1
	v_mfma_f32_32x32x16_f16 v[2:17], v[62:65], v[58:61], v[2:17]
	ds_read_b128 v[160:163], v159 offset:8928
	v_perm_b32 v155, v240, v152, s43
	v_perm_b32 v164, v240, v153, s42
	s_waitcnt lgkmcnt(0)
	v_mfma_f32_32x32x16_f16 v[18:33], v[66:69], v[160:163], v[18:33]
	v_perm_b32 v154, v240, v152, s42
	v_perm_b32 v165, v240, v153, s43
	v_pk_add_f16 v152, v154, s5 op_sel_hi:[1,0]
	v_pk_add_f16 v153, v155, s5 op_sel_hi:[1,0]
	v_pk_add_f16 v154, v164, s5 op_sel_hi:[1,0]
	v_pk_add_f16 v155, v165, s5 op_sel_hi:[1,0]
	v_mfma_f32_32x32x16_f16 v[34:49], v[160:163], v[74:77], v[34:49]
	v_perm_b32 v151, v240, v148, s43
	v_perm_b32 v164, v240, v149, s42
	v_mfma_f32_32x32x16_f16 v[18:33], v[54:57], v[152:155], v[18:33]
	v_perm_b32 v150, v240, v148, s42
	v_perm_b32 v165, v240, v149, s43
	v_pk_add_f16 v148, v150, s5 op_sel_hi:[1,0]
	v_pk_add_f16 v149, v151, s5 op_sel_hi:[1,0]
	v_pk_add_f16 v150, v164, s5 op_sel_hi:[1,0]
	v_pk_add_f16 v151, v165, s5 op_sel_hi:[1,0]
	s_nop 2
	v_cvt_pk_f16_f32 v41, v40, v41
	v_cvt_pk_f16_f32 v40, v38, v39
	v_cvt_pk_f16_f32 v38, v34, v35
	v_cvt_pk_f16_f32 v39, v36, v37
	v_mfma_f32_32x32x16_f16 v[18:33], v[62:65], v[148:151], v[18:33]
	v_perm_b32 v34, v240, v146, s42
	v_perm_b32 v35, v240, v146, s43
	v_perm_b32 v36, v240, v147, s42
	v_perm_b32 v37, v240, v147, s43
	v_pk_add_f16 v34, v34, s5 op_sel_hi:[1,0]
	v_pk_add_f16 v35, v35, s5 op_sel_hi:[1,0]
	v_pk_add_f16 v36, v36, s5 op_sel_hi:[1,0]
	v_pk_add_f16 v37, v37, s5 op_sel_hi:[1,0]
	v_perm_b32 v146, v240, v144, s42
	v_perm_b32 v144, v240, v144, s43
	v_perm_b32 v147, v240, v145, s42
	v_perm_b32 v53, v240, v145, s43
	v_pk_add_f16 v50, v146, s5 op_sel_hi:[1,0]
	v_pk_add_f16 v51, v144, s5 op_sel_hi:[1,0]
	v_pk_add_f16 v52, v147, s5 op_sel_hi:[1,0]
	v_pk_add_f16 v53, v53, s5 op_sel_hi:[1,0]
	v_cvt_pk_f16_f32 v49, v48, v49
	v_cvt_pk_f16_f32 v48, v46, v47
	v_cvt_pk_f16_f32 v47, v44, v45
	v_mfma_f32_32x32x16_f16 v[2:17], v[38:41], v[34:37], v[2:17]
	v_cvt_pk_f16_f32 v46, v42, v43
	v_mfma_f32_32x32x16_f16 v[18:33], v[38:41], v[50:53], v[18:33]
	v_perm_b32 v34, v240, v140, s42
	v_perm_b32 v35, v240, v140, s43
	v_perm_b32 v36, v240, v141, s42
	v_perm_b32 v37, v240, v141, s43
	v_perm_b32 v42, v240, v142, s42
	v_perm_b32 v43, v240, v142, s43
	v_perm_b32 v44, v240, v143, s42
	v_perm_b32 v45, v240, v143, s43
	v_pk_add_f16 v34, v34, s5 op_sel_hi:[1,0]
	v_pk_add_f16 v35, v35, s5 op_sel_hi:[1,0]
	v_pk_add_f16 v36, v36, s5 op_sel_hi:[1,0]
	v_pk_add_f16 v37, v37, s5 op_sel_hi:[1,0]
	v_pk_add_f16 v42, v42, s5 op_sel_hi:[1,0]
	v_pk_add_f16 v43, v43, s5 op_sel_hi:[1,0]
	v_pk_add_f16 v44, v44, s5 op_sel_hi:[1,0]
	v_pk_add_f16 v45, v45, s5 op_sel_hi:[1,0]
	v_mfma_f32_32x32x16_f16 v[18:33], v[46:49], v[34:37], v[18:33]
	global_load_dwordx2 v[154:155], v241, s[0:1] offset:2560
	global_load_dwordx2 v[152:153], v241, s[0:1] offset:3072
	global_load_dwordx2 v[150:151], v241, s[0:1] offset:3584
	v_mov_b32_e32 v148, v0
	s_or_b32 s0, s8, 4
	s_ashr_i32 s1, s0, 31
	s_lshl_b64 s[0:1], s[0:1], 12
	v_mfma_f32_32x32x16_f16 v[2:17], v[46:49], v[42:45], v[2:17]
	s_nop 7
	s_nop 4
	v_cvt_pk_f16_f32 v254, v2, v3
	v_cvt_pk_f16_f32 v255, v4, v5
	ds_write_b64 v251, v[254:255] offset:0
	v_cvt_pk_f16_f32 v252, v6, v7
	v_cvt_pk_f16_f32 v253, v8, v9
	ds_write_b64 v251, v[252:253] offset:16
	v_cvt_pk_f16_f32 v254, v10, v11
	v_cvt_pk_f16_f32 v255, v12, v13
	ds_write_b64 v251, v[254:255] offset:32
	v_cvt_pk_f16_f32 v252, v14, v15
	v_cvt_pk_f16_f32 v253, v16, v17
	ds_write_b64 v251, v[252:253] offset:48
	v_cvt_pk_f16_f32 v254, v18, v19
	v_cvt_pk_f16_f32 v255, v20, v21
	ds_write_b64 v251, v[254:255] offset:4608
	v_pk_add_f32 v[222:223], v[2:3], v[18:19]
	v_pk_mul_f32 v[194:195], v[2:3], v[2:3]
	v_pk_fma_f32 v[194:195], v[18:19], v[18:19], v[194:195]
	v_pk_add_f32 v[220:221], v[4:5], v[20:21]
	v_pk_mul_f32 v[192:193], v[4:5], v[4:5]
	v_pk_fma_f32 v[192:193], v[20:21], v[20:21], v[192:193]
	v_cvt_pk_f16_f32 v252, v22, v23
	v_cvt_pk_f16_f32 v253, v24, v25
	ds_write_b64 v251, v[252:253] offset:4624
	v_pk_add_f32 v[218:219], v[6:7], v[22:23]
	v_pk_mul_f32 v[184:185], v[6:7], v[6:7]
	v_pk_fma_f32 v[184:185], v[22:23], v[22:23], v[184:185]
	v_pk_add_f32 v[216:217], v[8:9], v[24:25]
	v_pk_mul_f32 v[166:167], v[8:9], v[8:9]
	v_pk_fma_f32 v[166:167], v[24:25], v[24:25], v[166:167]
	v_cvt_pk_f16_f32 v254, v26, v27
	v_cvt_pk_f16_f32 v255, v28, v29
	ds_write_b64 v251, v[254:255] offset:4640
	v_pk_add_f32 v[214:215], v[10:11], v[26:27]
	v_pk_mul_f32 v[164:165], v[10:11], v[10:11]
	v_pk_fma_f32 v[164:165], v[26:27], v[26:27], v[164:165]
	v_pk_add_f32 v[204:205], v[12:13], v[28:29]
	v_pk_mul_f32 v[162:163], v[12:13], v[12:13]
	v_pk_fma_f32 v[162:163], v[28:29], v[28:29], v[162:163]
	v_cvt_pk_f16_f32 v252, v30, v31
	v_cvt_pk_f16_f32 v253, v32, v33
	ds_write_b64 v251, v[252:253] offset:4656
	v_pk_add_f32 v[202:203], v[14:15], v[30:31]
	v_pk_mul_f32 v[160:161], v[14:15], v[14:15]
	v_pk_fma_f32 v[160:161], v[30:31], v[30:31], v[160:161]
	v_pk_add_f32 v[196:197], v[16:17], v[32:33]
	v_pk_mul_f32 v[156:157], v[16:17], v[16:17]
	v_pk_fma_f32 v[156:157], v[32:33], v[32:33], v[156:157]
	s_nop 3
	s_nop 0
	s_waitcnt lgkmcnt(0)
	s_barrier
	s_nop 4
	ds_read_b128 v[2:5], v159 offset:34816
	ds_read_b128 v[18:21], v159 offset:43520
	ds_read_b128 v[140:143], v159 offset:34848
	ds_read_b128 v[144:147], v159 offset:43552
	s_waitcnt lgkmcnt(3)
	v_mfma_f32_32x32x16_f16 v[50:65], v[2:5], v[126:129], 0
	s_add_u32 s0, s2, s0
	s_addc_u32 s1, s3, s1
	s_waitcnt lgkmcnt(2)
	v_mfma_f32_32x32x16_f16 v[34:49], v[18:21], v[126:129], 0
	v_mfma_f32_32x32x16_f16 v[2:17], v[122:125], v[2:5], v[168:183]
	v_mfma_f32_32x32x16_f16 v[18:33], v[122:125], v[18:21], v[168:183]
	ds_read_b128 v[242:245], v159 offset:34880
	ds_read_b128 v[246:249], v159 offset:43584
	s_waitcnt lgkmcnt(3)
	v_mfma_f32_32x32x16_f16 v[50:65], v[140:143], v[118:121], v[50:65]
	s_waitcnt lgkmcnt(2)
	v_mfma_f32_32x32x16_f16 v[34:49], v[144:147], v[118:121], v[34:49]
	v_mfma_f32_32x32x16_f16 v[2:17], v[114:117], v[140:143], v[2:17]
	v_mfma_f32_32x32x16_f16 v[18:33], v[114:117], v[144:147], v[18:33]
	ds_read_b128 v[140:143], v159 offset:34912
	ds_read_b128 v[144:147], v159 offset:43616
	s_waitcnt lgkmcnt(3)
	v_mfma_f32_32x32x16_f16 v[50:65], v[242:245], v[110:113], v[50:65]
	s_waitcnt lgkmcnt(2)
	v_mfma_f32_32x32x16_f16 v[34:49], v[246:249], v[110:113], v[34:49]
	v_mfma_f32_32x32x16_f16 v[2:17], v[106:109], v[242:245], v[2:17]
	v_mfma_f32_32x32x16_f16 v[18:33], v[106:109], v[246:249], v[18:33]
	ds_read_b128 v[242:245], v159 offset:34944
	ds_read_b128 v[246:249], v159 offset:43648
	s_waitcnt lgkmcnt(3)
	v_mfma_f32_32x32x16_f16 v[50:65], v[140:143], v[102:105], v[50:65]
	s_waitcnt lgkmcnt(2)
	v_mfma_f32_32x32x16_f16 v[34:49], v[144:147], v[102:105], v[34:49]
	v_mfma_f32_32x32x16_f16 v[2:17], v[98:101], v[140:143], v[2:17]
	v_mfma_f32_32x32x16_f16 v[18:33], v[98:101], v[144:147], v[18:33]
	ds_read_b128 v[186:189], v159 offset:34976
	ds_read_b128 v[206:209], v159 offset:43680
	s_waitcnt lgkmcnt(3)
	v_mfma_f32_32x32x16_f16 v[50:65], v[242:245], v[94:97], v[50:65]
	s_waitcnt lgkmcnt(2)
	v_mfma_f32_32x32x16_f16 v[34:49], v[246:249], v[94:97], v[34:49]
	v_mfma_f32_32x32x16_f16 v[2:17], v[86:89], v[242:245], v[2:17]
	v_mfma_f32_32x32x16_f16 v[18:33], v[86:89], v[246:249], v[18:33]
	ds_read_b128 v[140:143], v159 offset:35008
	ds_read_b128 v[144:147], v159 offset:43712
	s_waitcnt lgkmcnt(3)
	v_mfma_f32_32x32x16_f16 v[50:65], v[186:189], v[90:93], v[50:65]
	s_waitcnt lgkmcnt(2)
	v_mfma_f32_32x32x16_f16 v[34:49], v[206:209], v[90:93], v[34:49]
	v_mfma_f32_32x32x16_f16 v[2:17], v[78:81], v[186:189], v[2:17]
	v_mfma_f32_32x32x16_f16 v[18:33], v[78:81], v[206:209], v[18:33]
	ds_read_b128 v[186:189], v159 offset:35040
	ds_read_b128 v[206:209], v159 offset:43744
	s_waitcnt lgkmcnt(3)
	v_mfma_f32_32x32x16_f16 v[50:65], v[140:143], v[82:85], v[50:65]
	s_waitcnt lgkmcnt(2)
	v_mfma_f32_32x32x16_f16 v[34:49], v[144:147], v[82:85], v[34:49]
	v_mfma_f32_32x32x16_f16 v[2:17], v[70:73], v[140:143], v[2:17]
	v_lshlrev_b32_e32 v140, 3, v148
	v_and_b32_e32 v199, 0x1f8, v140
	global_load_dwordx2 v[148:149], v199, s[0:1]
	global_load_dwordx2 v[142:143], v199, s[0:1] offset:1024
	global_load_dwordx2 v[140:141], v199, s[0:1] offset:1536
	v_mfma_f32_32x32x16_f16 v[18:33], v[70:73], v[144:147], v[18:33]
	global_load_dwordx2 v[144:145], v199, s[0:1] offset:512
	global_load_dwordx2 v[146:147], v199, s[0:1] offset:2048
	s_waitcnt lgkmcnt(1)
	v_mfma_f32_32x32x16_f16 v[50:65], v[186:189], v[74:77], v[50:65]
	v_mfma_f32_32x32x16_f16 v[2:17], v[66:69], v[186:189], v[2:17]
	s_nop 10
	v_cvt_pk_f16_f32 v57, v56, v57
	v_cvt_pk_f16_f32 v56, v54, v55
	v_cvt_pk_f16_f32 v54, v50, v51
	s_waitcnt vmcnt(12)
	v_cvt_pk_f16_f32 v55, v52, v53
	s_waitcnt vmcnt(8)
	v_perm_b32 v50, v240, v138, s42
	v_perm_b32 v51, v240, v138, s43
	v_perm_b32 v52, v240, v139, s42
	v_perm_b32 v53, v240, v139, s43
	v_perm_b32 v139, v240, v136, s43
	v_pk_add_f16 v50, v50, s5 op_sel_hi:[1,0]
	v_pk_add_f16 v51, v51, s5 op_sel_hi:[1,0]
	v_pk_add_f16 v52, v52, s5 op_sel_hi:[1,0]
	v_pk_add_f16 v53, v53, s5 op_sel_hi:[1,0]
	v_perm_b32 v190, v240, v137, s42
	s_waitcnt lgkmcnt(0)
	v_mfma_f32_32x32x16_f16 v[18:33], v[66:69], v[206:209], v[18:33]
	v_perm_b32 v138, v240, v136, s42
	v_perm_b32 v191, v240, v137, s43
	v_pk_add_f16 v136, v138, s5 op_sel_hi:[1,0]
	v_pk_add_f16 v137, v139, s5 op_sel_hi:[1,0]
	v_pk_add_f16 v138, v190, s5 op_sel_hi:[1,0]
	v_pk_add_f16 v139, v191, s5 op_sel_hi:[1,0]
	v_cvt_pk_f16_f32 v65, v64, v65
	v_cvt_pk_f16_f32 v64, v62, v63
	v_cvt_pk_f16_f32 v63, v60, v61
	v_cvt_pk_f16_f32 v62, v58, v59
	v_mfma_f32_32x32x16_f16 v[34:49], v[206:209], v[74:77], v[34:49]
	v_mfma_f32_32x32x16_f16 v[2:17], v[54:57], v[50:53], v[2:17]
	s_waitcnt vmcnt(7)
	v_perm_b32 v58, v240, v134, s42
	v_perm_b32 v59, v240, v134, s43
	v_perm_b32 v60, v240, v135, s42
	v_perm_b32 v61, v240, v135, s43
	v_pk_add_f16 v58, v58, s5 op_sel_hi:[1,0]
	v_pk_add_f16 v59, v59, s5 op_sel_hi:[1,0]
	v_pk_add_f16 v60, v60, s5 op_sel_hi:[1,0]
	v_pk_add_f16 v61, v61, s5 op_sel_hi:[1,0]
	v_mfma_f32_32x32x16_f16 v[18:33], v[54:57], v[136:139], v[18:33]
	v_perm_b32 v134, v240, v154, s42
	v_perm_b32 v135, v240, v154, s43
	v_perm_b32 v154, v240, v155, s42
	v_perm_b32 v155, v240, v155, s43
	v_pk_add_f16 v210, v134, s5 op_sel_hi:[1,0]
	v_pk_add_f16 v211, v135, s5 op_sel_hi:[1,0]
	v_pk_add_f16 v212, v154, s5 op_sel_hi:[1,0]
	v_pk_add_f16 v213, v155, s5 op_sel_hi:[1,0]
	v_cvt_pk_f16_f32 v41, v40, v41
	v_cvt_pk_f16_f32 v40, v38, v39
	v_cvt_pk_f16_f32 v39, v36, v37
	v_cvt_pk_f16_f32 v38, v34, v35
	v_mfma_f32_32x32x16_f16 v[2:17], v[62:65], v[58:61], v[2:17]
	v_perm_b32 v34, v240, v132, s42
	v_perm_b32 v35, v240, v132, s43
	v_perm_b32 v36, v240, v133, s42
	v_perm_b32 v37, v240, v133, s43
	v_pk_add_f16 v34, v34, s5 op_sel_hi:[1,0]
	v_pk_add_f16 v35, v35, s5 op_sel_hi:[1,0]
	v_pk_add_f16 v36, v36, s5 op_sel_hi:[1,0]
	v_pk_add_f16 v37, v37, s5 op_sel_hi:[1,0]
	s_waitcnt vmcnt(6)
	v_mfma_f32_32x32x16_f16 v[18:33], v[62:65], v[210:213], v[18:33]
	v_perm_b32 v132, v240, v152, s42
	v_perm_b32 v133, v240, v152, s43
	v_perm_b32 v134, v240, v153, s42
	v_perm_b32 v53, v240, v153, s43
	v_pk_add_f16 v50, v132, s5 op_sel_hi:[1,0]
	v_pk_add_f16 v51, v133, s5 op_sel_hi:[1,0]
	v_pk_add_f16 v52, v134, s5 op_sel_hi:[1,0]
	v_pk_add_f16 v53, v53, s5 op_sel_hi:[1,0]
	v_cvt_pk_f16_f32 v49, v48, v49
	v_cvt_pk_f16_f32 v48, v46, v47
	v_cvt_pk_f16_f32 v47, v44, v45
	v_cvt_pk_f16_f32 v46, v42, v43
	v_mfma_f32_32x32x16_f16 v[2:17], v[38:41], v[34:37], v[2:17]
	v_perm_b32 v42, v240, v130, s42
	v_perm_b32 v43, v240, v130, s43
	v_perm_b32 v44, v240, v131, s42
	v_perm_b32 v45, v240, v131, s43
	v_pk_add_f16 v42, v42, s5 op_sel_hi:[1,0]
	v_pk_add_f16 v43, v43, s5 op_sel_hi:[1,0]
	v_pk_add_f16 v44, v44, s5 op_sel_hi:[1,0]
	v_pk_add_f16 v45, v45, s5 op_sel_hi:[1,0]
	s_waitcnt vmcnt(5)
	v_mfma_f32_32x32x16_f16 v[18:33], v[38:41], v[50:53], v[18:33]
	v_perm_b32 v34, v240, v150, s42
	v_perm_b32 v35, v240, v150, s43
	v_perm_b32 v36, v240, v151, s42
	v_perm_b32 v37, v240, v151, s43
	v_pk_add_f16 v34, v34, s5 op_sel_hi:[1,0]
	v_pk_add_f16 v35, v35, s5 op_sel_hi:[1,0]
	v_pk_add_f16 v36, v36, s5 op_sel_hi:[1,0]
	v_pk_add_f16 v37, v37, s5 op_sel_hi:[1,0]
	v_mfma_f32_32x32x16_f16 v[2:17], v[46:49], v[42:45], v[2:17]
	global_load_dwordx2 v[154:155], v199, s[0:1] offset:2560
	global_load_dwordx2 v[152:153], v199, s[0:1] offset:3072
	global_load_dwordx2 v[150:151], v199, s[0:1] offset:3584
	s_or_b32 s0, s8, 6
	s_ashr_i32 s1, s0, 31
	s_lshl_b64 s[0:1], s[0:1], 12
	s_add_u32 s0, s2, s0
	v_mfma_f32_32x32x16_f16 v[18:33], v[46:49], v[34:37], v[18:33]
	s_nop 7
	s_nop 4
	v_cvt_pk_f16_f32 v254, v2, v3
	v_cvt_pk_f16_f32 v255, v4, v5
	ds_write_b64 v251, v[254:255] offset:18432
	v_pk_add_f32 v[222:223], v[222:223], v[2:3]
	v_pk_fma_f32 v[194:195], v[2:3], v[2:3], v[194:195]
	v_pk_add_f32 v[220:221], v[220:221], v[4:5]
	v_pk_fma_f32 v[192:193], v[4:5], v[4:5], v[192:193]
	v_cvt_pk_f16_f32 v252, v6, v7
	v_cvt_pk_f16_f32 v253, v8, v9
	ds_write_b64 v251, v[252:253] offset:18448
	v_pk_add_f32 v[218:219], v[218:219], v[6:7]
	v_pk_fma_f32 v[184:185], v[6:7], v[6:7], v[184:185]
	v_pk_add_f32 v[216:217], v[216:217], v[8:9]
	v_pk_fma_f32 v[166:167], v[8:9], v[8:9], v[166:167]
	v_cvt_pk_f16_f32 v254, v10, v11
	v_cvt_pk_f16_f32 v255, v12, v13
	ds_write_b64 v251, v[254:255] offset:18464
	v_pk_add_f32 v[214:215], v[214:215], v[10:11]
	v_pk_fma_f32 v[164:165], v[10:11], v[10:11], v[164:165]
	v_pk_add_f32 v[204:205], v[204:205], v[12:13]
	v_pk_fma_f32 v[162:163], v[12:13], v[12:13], v[162:163]
	v_cvt_pk_f16_f32 v252, v14, v15
	v_cvt_pk_f16_f32 v253, v16, v17
	ds_write_b64 v251, v[252:253] offset:18480
	v_pk_add_f32 v[202:203], v[202:203], v[14:15]
	v_pk_fma_f32 v[160:161], v[14:15], v[14:15], v[160:161]
	v_pk_add_f32 v[196:197], v[196:197], v[16:17]
	v_pk_fma_f32 v[156:157], v[16:17], v[16:17], v[156:157]
	v_cvt_pk_f16_f32 v254, v18, v19
	v_cvt_pk_f16_f32 v255, v20, v21
	ds_write_b64 v251, v[254:255] offset:23040
	v_pk_add_f32 v[222:223], v[222:223], v[18:19]
	v_pk_fma_f32 v[194:195], v[18:19], v[18:19], v[194:195]
	v_pk_add_f32 v[220:221], v[220:221], v[20:21]
	v_pk_fma_f32 v[192:193], v[20:21], v[20:21], v[192:193]
	v_cvt_pk_f16_f32 v252, v22, v23
	v_cvt_pk_f16_f32 v253, v24, v25
	ds_write_b64 v251, v[252:253] offset:23056
	v_pk_add_f32 v[218:219], v[218:219], v[22:23]
	v_pk_fma_f32 v[184:185], v[22:23], v[22:23], v[184:185]
	v_pk_add_f32 v[216:217], v[216:217], v[24:25]
	v_pk_fma_f32 v[166:167], v[24:25], v[24:25], v[166:167]
	v_cvt_pk_f16_f32 v254, v26, v27
	v_cvt_pk_f16_f32 v255, v28, v29
	ds_write_b64 v251, v[254:255] offset:23072
	v_pk_add_f32 v[214:215], v[214:215], v[26:27]
	v_pk_fma_f32 v[164:165], v[26:27], v[26:27], v[164:165]
	v_pk_add_f32 v[204:205], v[204:205], v[28:29]
	v_pk_fma_f32 v[162:163], v[28:29], v[28:29], v[162:163]
	v_cvt_pk_f16_f32 v252, v30, v31
	v_cvt_pk_f16_f32 v253, v32, v33
	ds_write_b64 v251, v[252:253] offset:23088
	v_pk_add_f32 v[202:203], v[202:203], v[30:31]
	v_pk_fma_f32 v[160:161], v[30:31], v[30:31], v[160:161]
	v_pk_add_f32 v[196:197], v[196:197], v[32:33]
	v_pk_fma_f32 v[156:157], v[32:33], v[32:33], v[156:157]
	s_nop 3
	s_nop 0
	s_nop 0
	s_waitcnt lgkmcnt(0)
	s_barrier
	ds_read_b128 v[2:5], v159
	s_nop 2
	ds_read_b128 v[18:21], v159 offset:8704
	s_waitcnt lgkmcnt(1)
	v_mfma_f32_32x32x16_f16 v[50:65], v[2:5], v[126:129], 0
	v_lshlrev_b32_e32 v0, 3, v0
	s_addc_u32 s1, s3, s1
	v_and_b32_e32 v0, 0x1f8, v0
	global_load_dwordx2 v[138:139], v0, s[0:1]
	s_waitcnt lgkmcnt(0)
	v_mfma_f32_32x32x16_f16 v[34:49], v[18:21], v[126:129], 0
	v_mfma_f32_32x32x16_f16 v[2:17], v[122:125], v[2:5], v[168:183]
	v_mfma_f32_32x32x16_f16 v[18:33], v[122:125], v[18:21], v[168:183]
	ds_read_b128 v[130:133], v159 offset:32
	ds_read_b128 v[134:137], v159 offset:8736
	s_waitcnt lgkmcnt(1)
	v_mfma_f32_32x32x16_f16 v[50:65], v[130:133], v[118:121], v[50:65]
	s_waitcnt lgkmcnt(0)
	v_mfma_f32_32x32x16_f16 v[34:49], v[134:137], v[118:121], v[34:49]
	v_mfma_f32_32x32x16_f16 v[2:17], v[114:117], v[130:133], v[2:17]
	v_mfma_f32_32x32x16_f16 v[18:33], v[114:117], v[134:137], v[18:33]
	ds_read_b128 v[224:227], v159 offset:64
	ds_read_b128 v[228:231], v159 offset:8768
	ds_read_b128 v[130:133], v159 offset:96
	ds_read_b128 v[134:137], v159 offset:8800
	s_waitcnt lgkmcnt(3)
	v_mfma_f32_32x32x16_f16 v[50:65], v[224:227], v[110:113], v[50:65]
	s_waitcnt lgkmcnt(2)
	v_mfma_f32_32x32x16_f16 v[34:49], v[228:231], v[110:113], v[34:49]
	v_mfma_f32_32x32x16_f16 v[2:17], v[106:109], v[224:227], v[2:17]
	v_mfma_f32_32x32x16_f16 v[18:33], v[106:109], v[228:231], v[18:33]
	ds_read_b128 v[224:227], v159 offset:128
	ds_read_b128 v[228:231], v159 offset:8832
	s_waitcnt lgkmcnt(3)
	v_mfma_f32_32x32x16_f16 v[50:65], v[130:133], v[102:105], v[50:65]
	s_waitcnt lgkmcnt(2)
	v_mfma_f32_32x32x16_f16 v[34:49], v[134:137], v[102:105], v[34:49]
	v_mfma_f32_32x32x16_f16 v[2:17], v[98:101], v[130:133], v[2:17]
	v_mfma_f32_32x32x16_f16 v[18:33], v[98:101], v[134:137], v[18:33]
	ds_read_b128 v[130:133], v159 offset:160
	ds_read_b128 v[134:137], v159 offset:8864
	s_waitcnt lgkmcnt(3)
	v_mfma_f32_32x32x16_f16 v[50:65], v[224:227], v[94:97], v[50:65]
	s_waitcnt lgkmcnt(2)
	v_mfma_f32_32x32x16_f16 v[34:49], v[228:231], v[94:97], v[34:49]
	v_mfma_f32_32x32x16_f16 v[2:17], v[86:89], v[224:227], v[2:17]
	v_mfma_f32_32x32x16_f16 v[18:33], v[86:89], v[228:231], v[18:33]
	ds_read_b128 v[224:227], v159 offset:192
	ds_read_b128 v[228:231], v159 offset:8896
	s_waitcnt lgkmcnt(3)
	v_mfma_f32_32x32x16_f16 v[50:65], v[130:133], v[90:93], v[50:65]
	s_waitcnt lgkmcnt(2)
	v_mfma_f32_32x32x16_f16 v[34:49], v[134:137], v[90:93], v[34:49]
	v_mfma_f32_32x32x16_f16 v[2:17], v[78:81], v[130:133], v[2:17]
	v_mfma_f32_32x32x16_f16 v[18:33], v[78:81], v[134:137], v[18:33]
	ds_read_b128 v[232:235], v159 offset:224
	ds_read_b128 v[236:239], v159 offset:8928
	s_waitcnt lgkmcnt(3)
	v_mfma_f32_32x32x16_f16 v[50:65], v[224:227], v[82:85], v[50:65]
	global_load_dwordx2 v[134:135], v0, s[0:1] offset:512
	global_load_dwordx2 v[132:133], v0, s[0:1] offset:1024
	global_load_dwordx2 v[130:131], v0, s[0:1] offset:1536
	s_waitcnt lgkmcnt(2)
	v_mfma_f32_32x32x16_f16 v[34:49], v[228:231], v[82:85], v[34:49]
	global_load_dwordx2 v[136:137], v0, s[0:1] offset:2048
	v_mfma_f32_32x32x16_f16 v[2:17], v[70:73], v[224:227], v[2:17]
	v_mfma_f32_32x32x16_f16 v[18:33], v[70:73], v[228:231], v[18:33]
	s_waitcnt lgkmcnt(1)
	v_mfma_f32_32x32x16_f16 v[50:65], v[232:235], v[74:77], v[50:65]
	v_mfma_f32_32x32x16_f16 v[2:17], v[66:69], v[232:235], v[2:17]
	s_nop 10
	v_cvt_pk_f16_f32 v57, v56, v57
	v_cvt_pk_f16_f32 v56, v54, v55
	v_cvt_pk_f16_f32 v54, v50, v51
	s_waitcnt vmcnt(12)
	v_lshlrev_b32_e32 v50, 8, v148
	v_cvt_pk_f16_f32 v55, v52, v53
	v_perm_b32 v50, v50, v148, s4
	v_lshrrev_b32_e32 v51, 16, v148
	v_lshrrev_b32_e32 v52, 8, v148
	v_lshrrev_b32_e32 v53, 16, v149
	v_lshrrev_b32_e32 v148, 8, v149
	v_perm_b32 v51, v52, v51, s4
	v_lshlrev_b32_e32 v52, 8, v149
	v_perm_b32 v53, v148, v53, s4
	s_waitcnt vmcnt(8)
	v_perm_b32 v52, v52, v149, s4
	v_perm_b32 v149, v240, v146, s43
	v_perm_b32 v198, v240, v147, s42
	s_waitcnt lgkmcnt(0)
	v_mfma_f32_32x32x16_f16 v[18:33], v[66:69], v[236:239], v[18:33]
	v_or_b32_e32 v50, 0x64006400, v50
	v_or_b32_e32 v51, 0x64006400, v51
	v_or_b32_e32 v52, 0x64006400, v52
	v_or_b32_e32 v53, 0x64006400, v53
	v_pk_add_f16 v50, v50, s5 op_sel_hi:[1,0]
	v_pk_add_f16 v51, v51, s5 op_sel_hi:[1,0]
	v_pk_add_f16 v52, v52, s5 op_sel_hi:[1,0]
	v_pk_add_f16 v53, v53, s5 op_sel_hi:[1,0]
	v_perm_b32 v148, v240, v146, s42
	v_perm_b32 v200, v240, v147, s43
	v_pk_add_f16 v146, v148, s5 op_sel_hi:[1,0]
	v_pk_add_f16 v147, v149, s5 op_sel_hi:[1,0]
	v_pk_add_f16 v148, v198, s5 op_sel_hi:[1,0]
	v_pk_add_f16 v149, v200, s5 op_sel_hi:[1,0]
	v_cvt_pk_f16_f32 v65, v64, v65
	v_cvt_pk_f16_f32 v64, v62, v63
	v_cvt_pk_f16_f32 v62, v58, v59
	v_cvt_pk_f16_f32 v63, v60, v61
	s_waitcnt vmcnt(7)
	v_mfma_f32_32x32x16_f16 v[34:49], v[236:239], v[74:77], v[34:49]
	v_mfma_f32_32x32x16_f16 v[2:17], v[54:57], v[50:53], v[2:17]
	v_perm_b32 v58, v240, v144, s42
	v_perm_b32 v59, v240, v144, s43
	v_perm_b32 v60, v240, v145, s42
	v_perm_b32 v61, v240, v145, s43
	v_mfma_f32_32x32x16_f16 v[18:33], v[54:57], v[146:149], v[18:33]
	v_pk_add_f16 v58, v58, s5 op_sel_hi:[1,0]
	v_pk_add_f16 v59, v59, s5 op_sel_hi:[1,0]
	v_pk_add_f16 v60, v60, s5 op_sel_hi:[1,0]
	v_pk_add_f16 v61, v61, s5 op_sel_hi:[1,0]
	v_perm_b32 v144, v240, v154, s42
	v_perm_b32 v145, v240, v154, s43
	v_perm_b32 v154, v240, v155, s42
	v_perm_b32 v155, v240, v155, s43
	v_pk_add_f16 v224, v144, s5 op_sel_hi:[1,0]
	v_pk_add_f16 v225, v145, s5 op_sel_hi:[1,0]
	v_pk_add_f16 v226, v154, s5 op_sel_hi:[1,0]
	v_pk_add_f16 v227, v155, s5 op_sel_hi:[1,0]
	v_cvt_pk_f16_f32 v41, v40, v41
	v_cvt_pk_f16_f32 v40, v38, v39
	v_cvt_pk_f16_f32 v39, v36, v37
	v_cvt_pk_f16_f32 v38, v34, v35
	s_waitcnt vmcnt(6)
	v_mfma_f32_32x32x16_f16 v[2:17], v[62:65], v[58:61], v[2:17]
	v_perm_b32 v34, v240, v142, s42
	v_perm_b32 v35, v240, v142, s43
	v_mfma_f32_32x32x16_f16 v[18:33], v[62:65], v[224:227], v[18:33]
	v_perm_b32 v36, v240, v143, s42
	v_perm_b32 v37, v240, v143, s43
	v_pk_add_f16 v34, v34, s5 op_sel_hi:[1,0]
	v_pk_add_f16 v35, v35, s5 op_sel_hi:[1,0]
	v_pk_add_f16 v36, v36, s5 op_sel_hi:[1,0]
	v_pk_add_f16 v37, v37, s5 op_sel_hi:[1,0]
	v_perm_b32 v142, v240, v152, s42
	v_perm_b32 v143, v240, v152, s43
	v_perm_b32 v144, v240, v153, s42
	v_perm_b32 v53, v240, v153, s43
	v_pk_add_f16 v50, v142, s5 op_sel_hi:[1,0]
	v_pk_add_f16 v51, v143, s5 op_sel_hi:[1,0]
	v_pk_add_f16 v52, v144, s5 op_sel_hi:[1,0]
	v_pk_add_f16 v53, v53, s5 op_sel_hi:[1,0]
	v_cvt_pk_f16_f32 v49, v48, v49
	v_cvt_pk_f16_f32 v48, v46, v47
	v_cvt_pk_f16_f32 v47, v44, v45
	v_cvt_pk_f16_f32 v46, v42, v43
	v_mfma_f32_32x32x16_f16 v[2:17], v[38:41], v[34:37], v[2:17]
	s_waitcnt vmcnt(5)
	v_mfma_f32_32x32x16_f16 v[18:33], v[38:41], v[50:53], v[18:33]
	v_perm_b32 v42, v240, v140, s42
	v_perm_b32 v43, v240, v140, s43
	v_perm_b32 v44, v240, v141, s42
	v_perm_b32 v45, v240, v141, s43
	v_perm_b32 v34, v240, v150, s42
	v_perm_b32 v35, v240, v150, s43
	v_perm_b32 v36, v240, v151, s42
	v_perm_b32 v37, v240, v151, s43
	v_pk_add_f16 v42, v42, s5 op_sel_hi:[1,0]
	v_pk_add_f16 v43, v43, s5 op_sel_hi:[1,0]
	v_pk_add_f16 v44, v44, s5 op_sel_hi:[1,0]
	v_pk_add_f16 v45, v45, s5 op_sel_hi:[1,0]
	v_pk_add_f16 v34, v34, s5 op_sel_hi:[1,0]
	v_pk_add_f16 v35, v35, s5 op_sel_hi:[1,0]
	v_pk_add_f16 v36, v36, s5 op_sel_hi:[1,0]
	v_pk_add_f16 v37, v37, s5 op_sel_hi:[1,0]
	v_mfma_f32_32x32x16_f16 v[2:17], v[46:49], v[42:45], v[2:17]
	global_load_dwordx2 v[142:143], v0, s[0:1] offset:2560
	global_load_dwordx2 v[140:141], v0, s[0:1] offset:3072
	global_load_dwordx2 v[64:65], v0, s[0:1] offset:3584
	v_mfma_f32_32x32x16_f16 v[18:33], v[46:49], v[34:37], v[18:33]
	s_nop 7
	s_nop 4
	v_cvt_pk_f16_f32 v254, v2, v3
	v_cvt_pk_f16_f32 v255, v4, v5
	ds_write_b64 v251, v[254:255] offset:0
	v_pk_add_f32 v[222:223], v[222:223], v[2:3]
	v_pk_fma_f32 v[194:195], v[2:3], v[2:3], v[194:195]
	v_pk_add_f32 v[220:221], v[220:221], v[4:5]
	v_pk_fma_f32 v[192:193], v[4:5], v[4:5], v[192:193]
	v_cvt_pk_f16_f32 v252, v6, v7
	v_cvt_pk_f16_f32 v253, v8, v9
	ds_write_b64 v251, v[252:253] offset:16
	v_pk_add_f32 v[218:219], v[218:219], v[6:7]
	v_pk_fma_f32 v[184:185], v[6:7], v[6:7], v[184:185]
	v_pk_add_f32 v[216:217], v[216:217], v[8:9]
	v_pk_fma_f32 v[166:167], v[8:9], v[8:9], v[166:167]
	v_cvt_pk_f16_f32 v254, v10, v11
	v_cvt_pk_f16_f32 v255, v12, v13
	ds_write_b64 v251, v[254:255] offset:32
	v_pk_add_f32 v[214:215], v[214:215], v[10:11]
	v_pk_fma_f32 v[164:165], v[10:11], v[10:11], v[164:165]
	v_pk_add_f32 v[204:205], v[204:205], v[12:13]
	v_pk_fma_f32 v[162:163], v[12:13], v[12:13], v[162:163]
	v_cvt_pk_f16_f32 v252, v14, v15
	v_cvt_pk_f16_f32 v253, v16, v17
	ds_write_b64 v251, v[252:253] offset:48
	v_pk_add_f32 v[202:203], v[202:203], v[14:15]
	v_pk_fma_f32 v[160:161], v[14:15], v[14:15], v[160:161]
	v_pk_add_f32 v[196:197], v[196:197], v[16:17]
	v_pk_fma_f32 v[156:157], v[16:17], v[16:17], v[156:157]
	v_cvt_pk_f16_f32 v254, v18, v19
	v_cvt_pk_f16_f32 v255, v20, v21
	ds_write_b64 v251, v[254:255] offset:4608
	v_pk_add_f32 v[222:223], v[222:223], v[18:19]
	v_pk_fma_f32 v[194:195], v[18:19], v[18:19], v[194:195]
	v_pk_add_f32 v[220:221], v[220:221], v[20:21]
	v_pk_fma_f32 v[192:193], v[20:21], v[20:21], v[192:193]
	v_cvt_pk_f16_f32 v252, v22, v23
	v_cvt_pk_f16_f32 v253, v24, v25
	ds_write_b64 v251, v[252:253] offset:4624
	v_pk_add_f32 v[218:219], v[218:219], v[22:23]
	v_pk_fma_f32 v[184:185], v[22:23], v[22:23], v[184:185]
	v_pk_add_f32 v[216:217], v[216:217], v[24:25]
	v_pk_fma_f32 v[166:167], v[24:25], v[24:25], v[166:167]
	v_cvt_pk_f16_f32 v254, v26, v27
	v_cvt_pk_f16_f32 v255, v28, v29
	ds_write_b64 v251, v[254:255] offset:4640
	v_pk_add_f32 v[214:215], v[214:215], v[26:27]
	v_pk_fma_f32 v[164:165], v[26:27], v[26:27], v[164:165]
	v_pk_add_f32 v[204:205], v[204:205], v[28:29]
	v_pk_fma_f32 v[162:163], v[28:29], v[28:29], v[162:163]
	v_cvt_pk_f16_f32 v252, v30, v31
	v_cvt_pk_f16_f32 v253, v32, v33
	ds_write_b64 v251, v[252:253] offset:4656
	v_pk_add_f32 v[202:203], v[202:203], v[30:31]
	v_pk_fma_f32 v[160:161], v[30:31], v[30:31], v[160:161]
	v_pk_add_f32 v[196:197], v[196:197], v[32:33]
	v_pk_fma_f32 v[156:157], v[32:33], v[32:33], v[156:157]
	s_nop 7
	s_waitcnt lgkmcnt(0)
	s_barrier
	s_nop 1
	ds_read_b128 v[16:19], v159 offset:43520
	s_waitcnt lgkmcnt(0)
	v_mfma_f32_32x32x16_f16 v[32:47], v[16:19], v[126:129], 0
	ds_read_b128 v[2:5], v159 offset:34816
	s_waitcnt lgkmcnt(0)
	v_mfma_f32_32x32x16_f16 v[48:63], v[2:5], v[126:129], 0
	ds_read_b128 v[126:129], v159 offset:34848
	s_waitcnt lgkmcnt(0)
	v_mfma_f32_32x32x16_f16 v[48:63], v[126:129], v[118:121], v[48:63]
	v_mfma_f32_32x32x16_f16 v[0:15], v[122:125], v[2:5], v[168:183]
	v_mfma_f32_32x32x16_f16 v[0:15], v[114:117], v[126:129], v[0:15]
	v_mfma_f32_32x32x16_f16 v[16:31], v[122:125], v[16:19], v[168:183]
	ds_read_b128 v[122:125], v159 offset:43552
	s_waitcnt lgkmcnt(0)
	v_mfma_f32_32x32x16_f16 v[32:47], v[122:125], v[118:121], v[32:47]
	v_mfma_f32_32x32x16_f16 v[16:31], v[114:117], v[122:125], v[16:31]
	ds_read_b128 v[118:121], v159 offset:34880
	ds_read_b128 v[114:117], v159 offset:43584
	s_waitcnt lgkmcnt(1)
	v_mfma_f32_32x32x16_f16 v[48:63], v[118:121], v[110:113], v[48:63]
	s_waitcnt lgkmcnt(0)
	v_mfma_f32_32x32x16_f16 v[32:47], v[114:117], v[110:113], v[32:47]
	v_mfma_f32_32x32x16_f16 v[0:15], v[106:109], v[118:121], v[0:15]
	ds_read_b128 v[110:113], v159 offset:34912
	v_mfma_f32_32x32x16_f16 v[16:31], v[106:109], v[114:117], v[16:31]
	ds_read_b128 v[106:109], v159 offset:43616
	s_waitcnt lgkmcnt(1)
	v_mfma_f32_32x32x16_f16 v[48:63], v[110:113], v[102:105], v[48:63]
	s_waitcnt lgkmcnt(0)
	v_mfma_f32_32x32x16_f16 v[32:47], v[106:109], v[102:105], v[32:47]
	v_mfma_f32_32x32x16_f16 v[0:15], v[98:101], v[110:113], v[0:15]
	ds_read_b128 v[102:105], v159 offset:34944
	v_mfma_f32_32x32x16_f16 v[16:31], v[98:101], v[106:109], v[16:31]
	ds_read_b128 v[98:101], v159 offset:43648
	s_waitcnt lgkmcnt(1)
	v_mfma_f32_32x32x16_f16 v[48:63], v[102:105], v[94:97], v[48:63]
	s_waitcnt lgkmcnt(0)
	v_mfma_f32_32x32x16_f16 v[32:47], v[98:101], v[94:97], v[32:47]
	v_mfma_f32_32x32x16_f16 v[0:15], v[86:89], v[102:105], v[0:15]
	ds_read_b128 v[94:97], v159 offset:34976
	v_mfma_f32_32x32x16_f16 v[16:31], v[86:89], v[98:101], v[16:31]
	ds_read_b128 v[86:89], v159 offset:43680
	s_waitcnt lgkmcnt(1)
	v_mfma_f32_32x32x16_f16 v[48:63], v[94:97], v[90:93], v[48:63]
	s_waitcnt lgkmcnt(0)
	v_mfma_f32_32x32x16_f16 v[32:47], v[86:89], v[90:93], v[32:47]
	v_mfma_f32_32x32x16_f16 v[0:15], v[78:81], v[94:97], v[0:15]
	ds_read_b128 v[90:93], v159 offset:35008
	v_mfma_f32_32x32x16_f16 v[16:31], v[78:81], v[86:89], v[16:31]
	ds_read_b128 v[78:81], v159 offset:43712
	s_waitcnt lgkmcnt(1)
	v_mfma_f32_32x32x16_f16 v[48:63], v[90:93], v[82:85], v[48:63]
	s_waitcnt lgkmcnt(0)
	v_mfma_f32_32x32x16_f16 v[32:47], v[78:81], v[82:85], v[32:47]
	v_mfma_f32_32x32x16_f16 v[0:15], v[70:73], v[90:93], v[0:15]
	ds_read_b128 v[82:85], v159 offset:35040
	v_mfma_f32_32x32x16_f16 v[16:31], v[70:73], v[78:81], v[16:31]
	ds_read_b128 v[70:73], v159 offset:43744
	s_waitcnt lgkmcnt(1)
	v_mfma_f32_32x32x16_f16 v[48:63], v[82:85], v[74:77], v[48:63]
	v_mfma_f32_32x32x16_f16 v[0:15], v[66:69], v[82:85], v[0:15]
	s_nop 3
	s_nop 6
	v_cvt_pk_f16_f32 v55, v54, v55
	v_cvt_pk_f16_f32 v54, v52, v53
	v_cvt_pk_f16_f32 v53, v50, v51
	v_cvt_pk_f16_f32 v52, v48, v49
	s_waitcnt vmcnt(3)
	s_waitcnt lgkmcnt(0)
	v_mfma_f32_32x32x16_f16 v[16:31], v[66:69], v[70:73], v[16:31]
	v_lshrrev_b32_e32 v69, 16, v139
	v_mfma_f32_32x32x16_f16 v[32:47], v[70:73], v[74:77], v[32:47]
	v_lshrrev_b32_e32 v70, 8, v139
	v_perm_b32 v69, v70, v69, s4
	v_perm_b32 v66, v240, v138, s42
	v_perm_b32 v67, v240, v138, s43
	v_perm_b32 v68, v240, v139, s42
	v_or_b32_e32 v69, 0x64006400, v69
	v_pk_add_f16 v66, v66, s5 op_sel_hi:[1,0]
	v_pk_add_f16 v67, v67, s5 op_sel_hi:[1,0]
	v_pk_add_f16 v68, v68, s5 op_sel_hi:[1,0]
	v_pk_add_f16 v69, v69, s5 op_sel_hi:[1,0]
	s_nop 1
	v_mfma_f32_32x32x16_f16 v[0:15], v[52:55], v[66:69], v[0:15]
	v_perm_b32 v48, v240, v136, s42
	v_perm_b32 v49, v240, v136, s43
	v_perm_b32 v50, v240, v137, s42
	v_perm_b32 v51, v240, v137, s43
	v_pk_add_f16 v48, v48, s5 op_sel_hi:[1,0]
	v_pk_add_f16 v49, v49, s5 op_sel_hi:[1,0]
	v_pk_add_f16 v50, v50, s5 op_sel_hi:[1,0]
	v_pk_add_f16 v51, v51, s5 op_sel_hi:[1,0]
	v_cvt_pk_f16_f32 v39, v38, v39
	v_cvt_pk_f16_f32 v38, v36, v37
	v_mfma_f32_32x32x16_f16 v[16:31], v[52:55], v[48:51], v[16:31]
	v_perm_b32 v48, v240, v134, s42
	v_perm_b32 v49, v240, v134, s43
	v_perm_b32 v50, v240, v135, s42
	v_perm_b32 v51, v240, v135, s43
	v_pk_add_f16 v48, v48, s5 op_sel_hi:[1,0]
	v_pk_add_f16 v49, v49, s5 op_sel_hi:[1,0]
	v_pk_add_f16 v50, v50, s5 op_sel_hi:[1,0]
	v_pk_add_f16 v51, v51, s5 op_sel_hi:[1,0]
	v_cvt_pk_f16_f32 v55, v62, v63
	v_cvt_pk_f16_f32 v54, v60, v61
	v_cvt_pk_f16_f32 v53, v58, v59
	v_cvt_pk_f16_f32 v52, v56, v57
	s_waitcnt vmcnt(2)
	v_cvt_pk_f16_f32 v37, v34, v35
	v_mfma_f32_32x32x16_f16 v[0:15], v[52:55], v[48:51], v[0:15]
	v_perm_b32 v48, v240, v142, s42
	v_perm_b32 v49, v240, v142, s43
	v_perm_b32 v50, v240, v143, s42
	v_perm_b32 v51, v240, v143, s43
	v_pk_add_f16 v48, v48, s5 op_sel_hi:[1,0]
	v_pk_add_f16 v49, v49, s5 op_sel_hi:[1,0]
	v_pk_add_f16 v50, v50, s5 op_sel_hi:[1,0]
	v_pk_add_f16 v51, v51, s5 op_sel_hi:[1,0]
	v_cvt_pk_f16_f32 v36, v32, v33
	s_waitcnt vmcnt(1)
	v_mfma_f32_32x32x16_f16 v[16:31], v[52:55], v[48:51], v[16:31]
	v_lshrrev_b32_e32 v51, 16, v133
	v_lshrrev_b32_e32 v52, 8, v133
	v_perm_b32 v51, v52, v51, s4
	v_perm_b32 v48, v240, v132, s42
	v_perm_b32 v49, v240, v132, s43
	v_perm_b32 v50, v240, v133, s42
	v_or_b32_e32 v51, 0x64006400, v51
	v_pk_add_f16 v48, v48, s5 op_sel_hi:[1,0]
	v_pk_add_f16 v49, v49, s5 op_sel_hi:[1,0]
	v_pk_add_f16 v50, v50, s5 op_sel_hi:[1,0]
	v_pk_add_f16 v51, v51, s5 op_sel_hi:[1,0]
	s_nop 1
	v_mfma_f32_32x32x16_f16 v[0:15], v[36:39], v[48:51], v[0:15]
	v_perm_b32 v32, v240, v140, s42
	v_perm_b32 v33, v240, v140, s43
	v_perm_b32 v34, v240, v141, s42
	v_perm_b32 v35, v240, v141, s43
	v_pk_add_f16 v32, v32, s5 op_sel_hi:[1,0]
	v_pk_add_f16 v33, v33, s5 op_sel_hi:[1,0]
	v_pk_add_f16 v34, v34, s5 op_sel_hi:[1,0]
	v_pk_add_f16 v35, v35, s5 op_sel_hi:[1,0]
	s_nop 1
	v_mfma_f32_32x32x16_f16 v[16:31], v[36:39], v[32:35], v[16:31]
	v_perm_b32 v32, v240, v130, s42
	v_perm_b32 v33, v240, v130, s43
	v_perm_b32 v34, v240, v131, s42
	v_perm_b32 v35, v240, v131, s43
	v_pk_add_f16 v32, v32, s5 op_sel_hi:[1,0]
	v_pk_add_f16 v33, v33, s5 op_sel_hi:[1,0]
	v_pk_add_f16 v34, v34, s5 op_sel_hi:[1,0]
	v_pk_add_f16 v35, v35, s5 op_sel_hi:[1,0]
	v_cvt_pk_f16_f32 v39, v46, v47
	v_cvt_pk_f16_f32 v38, v44, v45
	v_cvt_pk_f16_f32 v37, v42, v43
	v_cvt_pk_f16_f32 v36, v40, v41
	s_waitcnt vmcnt(0)
	s_nop 0
	v_mfma_f32_32x32x16_f16 v[0:15], v[36:39], v[32:35], v[0:15]
	v_perm_b32 v32, v240, v64, s42
	v_perm_b32 v33, v240, v64, s43
	v_perm_b32 v34, v240, v65, s42
	v_perm_b32 v35, v240, v65, s43
	v_pk_add_f16 v32, v32, s5 op_sel_hi:[1,0]
	v_pk_add_f16 v33, v33, s5 op_sel_hi:[1,0]
	v_pk_add_f16 v34, v34, s5 op_sel_hi:[1,0]
	v_pk_add_f16 v35, v35, s5 op_sel_hi:[1,0]
	s_nop 3
	v_mfma_f32_32x32x16_f16 v[16:31], v[36:39], v[32:35], v[16:31]
	s_nop 7
	s_nop 4
	v_cvt_pk_f16_f32 v254, v0, v1
	v_cvt_pk_f16_f32 v255, v2, v3
	ds_write_b64 v251, v[254:255] offset:18432
	v_pk_add_f32 v[222:223], v[222:223], v[0:1]
	v_pk_fma_f32 v[194:195], v[0:1], v[0:1], v[194:195]
	v_pk_add_f32 v[220:221], v[220:221], v[2:3]
	v_pk_fma_f32 v[192:193], v[2:3], v[2:3], v[192:193]
	v_cvt_pk_f16_f32 v252, v4, v5
	v_cvt_pk_f16_f32 v253, v6, v7
	ds_write_b64 v251, v[252:253] offset:18448
	v_pk_add_f32 v[218:219], v[218:219], v[4:5]
	v_pk_fma_f32 v[184:185], v[4:5], v[4:5], v[184:185]
	v_pk_add_f32 v[216:217], v[216:217], v[6:7]
	v_pk_fma_f32 v[166:167], v[6:7], v[6:7], v[166:167]
	v_cvt_pk_f16_f32 v254, v8, v9
	v_cvt_pk_f16_f32 v255, v10, v11
	ds_write_b64 v251, v[254:255] offset:18464
	v_pk_add_f32 v[214:215], v[214:215], v[8:9]
	v_pk_fma_f32 v[164:165], v[8:9], v[8:9], v[164:165]
	v_pk_add_f32 v[204:205], v[204:205], v[10:11]
	v_pk_fma_f32 v[162:163], v[10:11], v[10:11], v[162:163]
	v_cvt_pk_f16_f32 v252, v12, v13
	v_cvt_pk_f16_f32 v253, v14, v15
	ds_write_b64 v251, v[252:253] offset:18480
	v_pk_add_f32 v[202:203], v[202:203], v[12:13]
	v_pk_fma_f32 v[160:161], v[12:13], v[12:13], v[160:161]
	v_pk_add_f32 v[196:197], v[196:197], v[14:15]
	v_pk_fma_f32 v[156:157], v[14:15], v[14:15], v[156:157]
	v_cvt_pk_f16_f32 v254, v16, v17
	v_cvt_pk_f16_f32 v255, v18, v19
	ds_write_b64 v251, v[254:255] offset:23040
	v_pk_add_f32 v[222:223], v[222:223], v[16:17]
	v_pk_fma_f32 v[194:195], v[16:17], v[16:17], v[194:195]
	v_pk_add_f32 v[220:221], v[220:221], v[18:19]
	v_pk_fma_f32 v[192:193], v[18:19], v[18:19], v[192:193]
	v_cvt_pk_f16_f32 v252, v20, v21
	v_cvt_pk_f16_f32 v253, v22, v23
	ds_write_b64 v251, v[252:253] offset:23056
	v_pk_add_f32 v[218:219], v[218:219], v[20:21]
	v_pk_fma_f32 v[184:185], v[20:21], v[20:21], v[184:185]
	v_pk_add_f32 v[216:217], v[216:217], v[22:23]
	v_pk_fma_f32 v[166:167], v[22:23], v[22:23], v[166:167]
	v_cvt_pk_f16_f32 v254, v24, v25
	v_cvt_pk_f16_f32 v255, v26, v27
	ds_write_b64 v251, v[254:255] offset:23072
	v_pk_add_f32 v[214:215], v[214:215], v[24:25]
	v_pk_fma_f32 v[164:165], v[24:25], v[24:25], v[164:165]
	v_pk_add_f32 v[204:205], v[204:205], v[26:27]
	v_pk_fma_f32 v[162:163], v[26:27], v[26:27], v[162:163]
	v_cvt_pk_f16_f32 v252, v28, v29
	v_cvt_pk_f16_f32 v253, v30, v31
	ds_write_b64 v251, v[252:253] offset:23088
	v_pk_add_f32 v[202:203], v[202:203], v[28:29]
	v_pk_fma_f32 v[160:161], v[28:29], v[28:29], v[160:161]
	v_pk_add_f32 v[196:197], v[196:197], v[30:31]
	v_pk_fma_f32 v[156:157], v[30:31], v[30:31], v[156:157]
	s_nop 4
	s_nop 0
	v_add_f32_dpp v222, v222, v222 row_half_mirror row_mask:0xf bank_mask:0x5
	v_add_f32_dpp v222, v223, v223 row_half_mirror row_mask:0xf bank_mask:0xa
	v_add_f32_dpp v220, v220, v220 row_half_mirror row_mask:0xf bank_mask:0x5
	v_add_f32_dpp v220, v221, v221 row_half_mirror row_mask:0xf bank_mask:0xa
	v_add_f32_dpp v218, v218, v218 row_half_mirror row_mask:0xf bank_mask:0x5
	v_add_f32_dpp v218, v219, v219 row_half_mirror row_mask:0xf bank_mask:0xa
	v_add_f32_dpp v216, v216, v216 row_half_mirror row_mask:0xf bank_mask:0x5
	v_add_f32_dpp v216, v217, v217 row_half_mirror row_mask:0xf bank_mask:0xa
	v_add_f32_dpp v214, v214, v214 row_half_mirror row_mask:0xf bank_mask:0x5
	v_add_f32_dpp v214, v215, v215 row_half_mirror row_mask:0xf bank_mask:0xa
	v_add_f32_dpp v204, v204, v204 row_half_mirror row_mask:0xf bank_mask:0x5
	v_add_f32_dpp v204, v205, v205 row_half_mirror row_mask:0xf bank_mask:0xa
	v_add_f32_dpp v202, v202, v202 row_half_mirror row_mask:0xf bank_mask:0x5
	v_add_f32_dpp v202, v203, v203 row_half_mirror row_mask:0xf bank_mask:0xa
	v_add_f32_dpp v196, v196, v196 row_half_mirror row_mask:0xf bank_mask:0x5
	v_add_f32_dpp v196, v197, v197 row_half_mirror row_mask:0xf bank_mask:0xa
	v_add_f32_dpp v194, v194, v194 row_half_mirror row_mask:0xf bank_mask:0x5
	v_add_f32_dpp v194, v195, v195 row_half_mirror row_mask:0xf bank_mask:0xa
	v_add_f32_dpp v192, v192, v192 row_half_mirror row_mask:0xf bank_mask:0x5
	v_add_f32_dpp v192, v193, v193 row_half_mirror row_mask:0xf bank_mask:0xa
	v_add_f32_dpp v184, v184, v184 row_half_mirror row_mask:0xf bank_mask:0x5
	v_add_f32_dpp v184, v185, v185 row_half_mirror row_mask:0xf bank_mask:0xa
	v_add_f32_dpp v166, v166, v166 row_half_mirror row_mask:0xf bank_mask:0x5
	v_add_f32_dpp v166, v167, v167 row_half_mirror row_mask:0xf bank_mask:0xa
	v_add_f32_dpp v164, v164, v164 row_half_mirror row_mask:0xf bank_mask:0x5
	v_add_f32_dpp v164, v165, v165 row_half_mirror row_mask:0xf bank_mask:0xa
	v_add_f32_dpp v162, v162, v162 row_half_mirror row_mask:0xf bank_mask:0x5
	v_add_f32_dpp v162, v163, v163 row_half_mirror row_mask:0xf bank_mask:0xa
	v_add_f32_dpp v160, v160, v160 row_half_mirror row_mask:0xf bank_mask:0x5
	v_add_f32_dpp v160, v161, v161 row_half_mirror row_mask:0xf bank_mask:0xa
	v_add_f32_dpp v156, v156, v156 row_half_mirror row_mask:0xf bank_mask:0x5
	v_add_f32_dpp v156, v157, v157 row_half_mirror row_mask:0xf bank_mask:0xa
	v_add_f32_dpp v222, v222, v222 row_ror:8 row_mask:0xf bank_mask:0x3
	v_add_f32_dpp v222, v220, v220 row_ror:8 row_mask:0xf bank_mask:0xc
	v_add_f32_dpp v218, v218, v218 row_ror:8 row_mask:0xf bank_mask:0x3
	v_add_f32_dpp v218, v216, v216 row_ror:8 row_mask:0xf bank_mask:0xc
	v_add_f32_dpp v214, v214, v214 row_ror:8 row_mask:0xf bank_mask:0x3
	v_add_f32_dpp v214, v204, v204 row_ror:8 row_mask:0xf bank_mask:0xc
	v_add_f32_dpp v202, v202, v202 row_ror:8 row_mask:0xf bank_mask:0x3
	v_add_f32_dpp v202, v196, v196 row_ror:8 row_mask:0xf bank_mask:0xc
	v_add_f32_dpp v194, v194, v194 row_ror:8 row_mask:0xf bank_mask:0x3
	v_add_f32_dpp v194, v192, v192 row_ror:8 row_mask:0xf bank_mask:0xc
	v_add_f32_dpp v184, v184, v184 row_ror:8 row_mask:0xf bank_mask:0x3
	v_add_f32_dpp v184, v166, v166 row_ror:8 row_mask:0xf bank_mask:0xc
	v_add_f32_dpp v164, v164, v164 row_ror:8 row_mask:0xf bank_mask:0x3
	v_add_f32_dpp v164, v162, v162 row_ror:8 row_mask:0xf bank_mask:0xc
	v_add_f32_dpp v160, v160, v160 row_ror:8 row_mask:0xf bank_mask:0x3
	v_add_f32_dpp v160, v156, v156 row_ror:8 row_mask:0xf bank_mask:0xc
	v_add_f32_dpp v222, v222, v222 quad_perm:[1,0,3,2] row_mask:0xf bank_mask:0xf
	v_add_f32_dpp v218, v218, v218 quad_perm:[1,0,3,2] row_mask:0xf bank_mask:0xf
	v_add_f32_dpp v214, v214, v214 quad_perm:[1,0,3,2] row_mask:0xf bank_mask:0xf
	v_add_f32_dpp v202, v202, v202 quad_perm:[1,0,3,2] row_mask:0xf bank_mask:0xf
	v_add_f32_dpp v194, v194, v194 quad_perm:[1,0,3,2] row_mask:0xf bank_mask:0xf
	v_add_f32_dpp v184, v184, v184 quad_perm:[1,0,3,2] row_mask:0xf bank_mask:0xf
	v_add_f32_dpp v164, v164, v164 quad_perm:[1,0,3,2] row_mask:0xf bank_mask:0xf
	v_add_f32_dpp v160, v160, v160 quad_perm:[1,0,3,2] row_mask:0xf bank_mask:0xf
	v_add_f32_dpp v222, v222, v222 quad_perm:[2,3,0,1] row_mask:0xf bank_mask:0xf
	v_add_f32_dpp v218, v218, v218 quad_perm:[2,3,0,1] row_mask:0xf bank_mask:0xf
	v_add_f32_dpp v214, v214, v214 quad_perm:[2,3,0,1] row_mask:0xf bank_mask:0xf
	v_add_f32_dpp v202, v202, v202 quad_perm:[2,3,0,1] row_mask:0xf bank_mask:0xf
	v_add_f32_dpp v194, v194, v194 quad_perm:[2,3,0,1] row_mask:0xf bank_mask:0xf
	v_add_f32_dpp v184, v184, v184 quad_perm:[2,3,0,1] row_mask:0xf bank_mask:0xf
	v_add_f32_dpp v164, v164, v164 quad_perm:[2,3,0,1] row_mask:0xf bank_mask:0xf
	v_add_f32_dpp v160, v160, v160 quad_perm:[2,3,0,1] row_mask:0xf bank_mask:0xf
	s_mov_b32 exec_lo, 0x1111
	s_mov_b32 exec_hi, 0x1111
	ds_add_f32 v250, v222 offset:0
	ds_add_f32 v250, v218 offset:32
	ds_add_f32 v250, v214 offset:64
	ds_add_f32 v250, v202 offset:96
	ds_add_f32 v250, v194 offset:256
	ds_add_f32 v250, v184 offset:288
	ds_add_f32 v250, v164 offset:320
	ds_add_f32 v250, v160 offset:352
	s_waitcnt lgkmcnt(7)
	s_mov_b32 exec_lo, 0x11110000
	s_mov_b32 exec_hi, 0x11110000
	ds_add_f32 v250, v222 offset:0
	ds_add_f32 v250, v218 offset:32
	ds_add_f32 v250, v214 offset:64
	ds_add_f32 v250, v202 offset:96
	ds_add_f32 v250, v194 offset:256
	ds_add_f32 v250, v184 offset:288
	ds_add_f32 v250, v164 offset:320
	ds_add_f32 v250, v160 offset:352
	s_mov_b64 exec, -1
	s_waitcnt lgkmcnt(0)
	s_barrier
	s_cmp_lg_u32 s50, 0
	s_cbranch_scc1 .LBB2_27
	v_mbcnt_lo_u32_b32 v2, -1, 0
	v_mbcnt_hi_u32_b32 v2, -1, v2
	v_and_b32_e32 v3, 32, v2
	v_add_u32_e32 v4, v2, v3
	v_lshl_add_u32 v5, v4, 2, s49
	ds_read_b32 v6, v5
	v_lshl_add_u32 v4, v3, 1, v4
	v_add_u32_e32 v4, s48, v4
	v_lshlrev_b32_e32 v4, 2, v4
	s_waitcnt lgkmcnt(0)
	global_atomic_add_f32 v4, v6, s[46:47]

.LBB3_24:
	s_or_b64 exec, exec, s[2:3]
	v_and_b32_e32 v1, 31, v0
	v_lshlrev_b32_e32 v2, 2, v1
	v_lshl_or_b32 v2, s13, 7, v2
	v_or_b32_e32 v2, 0x1ee00, v2
	v_lshrrev_b32_e32 v158, 5, v156
	s_waitcnt lgkmcnt(0)
	s_barrier
	v_lshlrev_b32_e32 v250, 4, v158
	v_lshl_or_b32 v250, s13, 7, v250
	v_or_b32_e32 v254, 0x1ee00, v250
	ds_read_b128 v[168:171], v254 offset:0
	ds_read_b128 v[172:175], v254 offset:32
	ds_read_b128 v[176:179], v254 offset:64
	ds_read_b128 v[180:183], v254 offset:96
	v_bfe_u32 v255, v156, 2, 2
	v_lshl_add_u32 v250, v255, 2, v250
	v_add_u32_e32 v250, 0x1e400, v250
	s_waitcnt lgkmcnt(0)
	s_barrier
	ds_read_b32 v157, v2
	v_mul_u32_u24_e32 v2, 0x88, v1
	s_mul_i32 s0, s16, 0x4400
	v_lshlrev_b32_e32 v2, 1, v2
	v_lshlrev_b32_e32 v3, 4, v158
	v_mov_b32_e32 v138, v0
	v_add3_u32 v159, s0, v2, v3
	ds_read_b128 v[2:5], v159
	ds_read_b128 v[18:21], v159 offset:8704
	ds_read_b128 v[130:133], v159 offset:32
	s_waitcnt vmcnt(10) lgkmcnt(2)
	v_mfma_f32_32x32x16_f16 v[50:65], v[2:5], v[126:129], 0
	s_mov_b32 s2, 0xc060c00
	s_mov_b32 s3, 0xe400
	s_mulk_i32 s16, 0x2400
	s_lshl_b32 s0, s13, 6
	s_or_b32 s0, s16, s0
	s_add_i32 s0, s0, 0x11000
	v_mul_u32_u24_e32 v251, 0x90, v1
	v_lshl_add_u32 v251, v158, 3, v251
	v_add_u32_e32 v251, s0, v251
	s_waitcnt lgkmcnt(1)
	v_mfma_f32_32x32x16_f16 v[34:49], v[18:21], v[126:129], 0
	s_or_b32 s0, s10, 2
	s_ashr_i32 s1, s0, 31
	s_lshl_b64 s[0:1], s[0:1], 12
	s_add_u32 s0, s8, s0
	s_addc_u32 s1, s9, s1
	v_cmp_gt_u32_e32 vcc, 32, v156
	v_mfma_f32_32x32x16_f16 v[2:17], v[122:125], v[2:5], v[168:183]
	v_mfma_f32_32x32x16_f16 v[18:33], v[122:125], v[18:21], v[168:183]
	ds_read_b128 v[134:137], v159 offset:8736
	ds_read_b128 v[160:163], v159 offset:64
	s_waitcnt vmcnt(8) lgkmcnt(2)
	v_mfma_f32_32x32x16_f16 v[50:65], v[130:133], v[118:121], v[50:65]
	s_waitcnt lgkmcnt(1)
	v_mfma_f32_32x32x16_f16 v[34:49], v[134:137], v[118:121], v[34:49]
	v_mfma_f32_32x32x16_f16 v[2:17], v[114:117], v[130:133], v[2:17]
	v_mfma_f32_32x32x16_f16 v[18:33], v[114:117], v[134:137], v[18:33]
	ds_read_b128 v[130:133], v159 offset:8768
	ds_read_b128 v[134:137], v159 offset:96
	s_waitcnt vmcnt(6) lgkmcnt(2)
	v_mfma_f32_32x32x16_f16 v[50:65], v[160:163], v[110:113], v[50:65]
	s_waitcnt lgkmcnt(1)
	v_mfma_f32_32x32x16_f16 v[34:49], v[130:133], v[110:113], v[34:49]
	v_mfma_f32_32x32x16_f16 v[2:17], v[106:109], v[160:163], v[2:17]
	v_mfma_f32_32x32x16_f16 v[18:33], v[106:109], v[130:133], v[18:33]
	ds_read_b128 v[130:133], v159 offset:8800
	ds_read_b128 v[160:163], v159 offset:128
	s_waitcnt vmcnt(4) lgkmcnt(2)
	v_mfma_f32_32x32x16_f16 v[50:65], v[134:137], v[102:105], v[50:65]
	s_waitcnt lgkmcnt(1)
	v_mfma_f32_32x32x16_f16 v[34:49], v[130:133], v[102:105], v[34:49]
	v_mfma_f32_32x32x16_f16 v[2:17], v[98:101], v[134:137], v[2:17]
	v_mfma_f32_32x32x16_f16 v[18:33], v[98:101], v[130:133], v[18:33]
	ds_read_b128 v[130:133], v159 offset:8832
	ds_read_b128 v[134:137], v159 offset:160
	s_waitcnt vmcnt(3) lgkmcnt(2)
	v_mfma_f32_32x32x16_f16 v[50:65], v[160:163], v[94:97], v[50:65]
	s_waitcnt lgkmcnt(1)
	v_mfma_f32_32x32x16_f16 v[34:49], v[130:133], v[94:97], v[34:49]
	v_mfma_f32_32x32x16_f16 v[2:17], v[86:89], v[160:163], v[2:17]
	v_mfma_f32_32x32x16_f16 v[18:33], v[86:89], v[130:133], v[18:33]
	ds_read_b128 v[130:133], v159 offset:8864
	ds_read_b128 v[160:163], v159 offset:192
	s_waitcnt vmcnt(2) lgkmcnt(2)
	v_mfma_f32_32x32x16_f16 v[50:65], v[134:137], v[90:93], v[50:65]
	s_waitcnt lgkmcnt(1)
	v_mfma_f32_32x32x16_f16 v[34:49], v[130:133], v[90:93], v[34:49]
	v_mfma_f32_32x32x16_f16 v[2:17], v[78:81], v[134:137], v[2:17]
	v_mfma_f32_32x32x16_f16 v[18:33], v[78:81], v[130:133], v[18:33]
	ds_read_b128 v[130:133], v159 offset:8896
	ds_read_b128 v[164:167], v159 offset:224
	s_waitcnt vmcnt(1) lgkmcnt(2)
	v_mfma_f32_32x32x16_f16 v[50:65], v[160:163], v[82:85], v[50:65]
	s_waitcnt lgkmcnt(1)
	v_mfma_f32_32x32x16_f16 v[34:49], v[130:133], v[82:85], v[34:49]
	v_mfma_f32_32x32x16_f16 v[2:17], v[70:73], v[160:163], v[2:17]
	v_mfma_f32_32x32x16_f16 v[18:33], v[70:73], v[130:133], v[18:33]
	v_lshlrev_b32_e32 v130, 3, v138
	v_and_b32_e32 v241, 0x1f8, v130
	global_load_dwordx2 v[138:139], v241, s[0:1]
	global_load_dwordx2 v[134:135], v241, s[0:1] offset:512
	global_load_dwordx2 v[132:133], v241, s[0:1] offset:1024
	global_load_dwordx2 v[130:131], v241, s[0:1] offset:1536
	global_load_dwordx2 v[136:137], v241, s[0:1] offset:2048
	s_waitcnt vmcnt(5) lgkmcnt(0)
	v_mfma_f32_32x32x16_f16 v[50:65], v[164:167], v[74:77], v[50:65]
	v_mfma_f32_32x32x16_f16 v[2:17], v[66:69], v[164:167], v[2:17]
	s_nop 10
	v_cvt_pk_f16_f32 v57, v56, v57
	v_cvt_pk_f16_f32 v56, v54, v55
	v_cvt_pk_f16_f32 v55, v52, v53
	v_cvt_pk_f16_f32 v54, v50, v51
	v_perm_b32 v50, v240, v154, s42
	v_perm_b32 v51, v240, v154, s43
	v_perm_b32 v52, v240, v155, s42
	v_perm_b32 v53, v240, v155, s43
	v_pk_add_f16 v50, v50, s3 op_sel_hi:[1,0]
	v_pk_add_f16 v51, v51, s3 op_sel_hi:[1,0]
	v_pk_add_f16 v52, v52, s3 op_sel_hi:[1,0]
	v_pk_add_f16 v53, v53, s3 op_sel_hi:[1,0]
	v_cvt_pk_f16_f32 v65, v64, v65
	v_cvt_pk_f16_f32 v64, v62, v63
	v_cvt_pk_f16_f32 v63, v60, v61
	v_cvt_pk_f16_f32 v62, v58, v59
	v_mfma_f32_32x32x16_f16 v[2:17], v[54:57], v[50:53], v[2:17]
	v_perm_b32 v58, v240, v150, s42
	v_perm_b32 v59, v240, v150, s43
	v_perm_b32 v60, v240, v151, s42
	v_perm_b32 v61, v240, v151, s43
	v_pk_add_f16 v58, v58, s3 op_sel_hi:[1,0]
	v_pk_add_f16 v59, v59, s3 op_sel_hi:[1,0]
	v_pk_add_f16 v60, v60, s3 op_sel_hi:[1,0]
	v_pk_add_f16 v61, v61, s3 op_sel_hi:[1,0]
	s_nop 1
	v_mfma_f32_32x32x16_f16 v[2:17], v[62:65], v[58:61], v[2:17]
	ds_read_b128 v[160:163], v159 offset:8928
	v_perm_b32 v155, v240, v152, s43
	v_perm_b32 v164, v240, v153, s42
	s_waitcnt lgkmcnt(0)
	v_mfma_f32_32x32x16_f16 v[18:33], v[66:69], v[160:163], v[18:33]
	v_perm_b32 v154, v240, v152, s42
	v_perm_b32 v165, v240, v153, s43
	v_pk_add_f16 v152, v154, s3 op_sel_hi:[1,0]
	v_pk_add_f16 v153, v155, s3 op_sel_hi:[1,0]
	v_pk_add_f16 v154, v164, s3 op_sel_hi:[1,0]
	v_pk_add_f16 v155, v165, s3 op_sel_hi:[1,0]
	v_mfma_f32_32x32x16_f16 v[34:49], v[160:163], v[74:77], v[34:49]
	v_perm_b32 v151, v240, v148, s43
	v_perm_b32 v164, v240, v149, s42
	v_mfma_f32_32x32x16_f16 v[18:33], v[54:57], v[152:155], v[18:33]
	v_perm_b32 v150, v240, v148, s42
	v_perm_b32 v165, v240, v149, s43
	v_pk_add_f16 v148, v150, s3 op_sel_hi:[1,0]
	v_pk_add_f16 v149, v151, s3 op_sel_hi:[1,0]
	v_pk_add_f16 v150, v164, s3 op_sel_hi:[1,0]
	v_pk_add_f16 v151, v165, s3 op_sel_hi:[1,0]
	s_nop 2
	v_cvt_pk_f16_f32 v41, v40, v41
	v_cvt_pk_f16_f32 v40, v38, v39
	v_cvt_pk_f16_f32 v38, v34, v35
	v_cvt_pk_f16_f32 v39, v36, v37
	v_mfma_f32_32x32x16_f16 v[18:33], v[62:65], v[148:151], v[18:33]
	v_perm_b32 v34, v240, v146, s42
	v_perm_b32 v35, v240, v146, s43
	v_perm_b32 v36, v240, v147, s42
	v_perm_b32 v37, v240, v147, s43
	v_pk_add_f16 v34, v34, s3 op_sel_hi:[1,0]
	v_pk_add_f16 v35, v35, s3 op_sel_hi:[1,0]
	v_pk_add_f16 v36, v36, s3 op_sel_hi:[1,0]
	v_pk_add_f16 v37, v37, s3 op_sel_hi:[1,0]
	v_perm_b32 v146, v240, v144, s42
	v_perm_b32 v144, v240, v144, s43
	v_perm_b32 v147, v240, v145, s42
	v_perm_b32 v53, v240, v145, s43
	v_pk_add_f16 v50, v146, s3 op_sel_hi:[1,0]
	v_pk_add_f16 v51, v144, s3 op_sel_hi:[1,0]
	v_pk_add_f16 v52, v147, s3 op_sel_hi:[1,0]
	v_pk_add_f16 v53, v53, s3 op_sel_hi:[1,0]
	v_cvt_pk_f16_f32 v49, v48, v49
	v_cvt_pk_f16_f32 v48, v46, v47
	v_cvt_pk_f16_f32 v47, v44, v45
	v_mfma_f32_32x32x16_f16 v[2:17], v[38:41], v[34:37], v[2:17]
	v_cvt_pk_f16_f32 v46, v42, v43
	v_mfma_f32_32x32x16_f16 v[18:33], v[38:41], v[50:53], v[18:33]
	v_perm_b32 v34, v240, v140, s42
	v_perm_b32 v35, v240, v140, s43
	v_perm_b32 v36, v240, v141, s42
	v_perm_b32 v37, v240, v141, s43
	v_perm_b32 v42, v240, v142, s42
	v_perm_b32 v43, v240, v142, s43
	v_perm_b32 v44, v240, v143, s42
	v_perm_b32 v45, v240, v143, s43
	v_pk_add_f16 v34, v34, s3 op_sel_hi:[1,0]
	v_pk_add_f16 v35, v35, s3 op_sel_hi:[1,0]
	v_pk_add_f16 v36, v36, s3 op_sel_hi:[1,0]
	v_pk_add_f16 v37, v37, s3 op_sel_hi:[1,0]
	v_pk_add_f16 v42, v42, s3 op_sel_hi:[1,0]
	v_pk_add_f16 v43, v43, s3 op_sel_hi:[1,0]
	v_pk_add_f16 v44, v44, s3 op_sel_hi:[1,0]
	v_pk_add_f16 v45, v45, s3 op_sel_hi:[1,0]
	v_mfma_f32_32x32x16_f16 v[18:33], v[46:49], v[34:37], v[18:33]
	global_load_dwordx2 v[154:155], v241, s[0:1] offset:2560
	global_load_dwordx2 v[152:153], v241, s[0:1] offset:3072
	global_load_dwordx2 v[150:151], v241, s[0:1] offset:3584
	v_mov_b32_e32 v148, v0
	s_or_b32 s0, s10, 4
	s_ashr_i32 s1, s0, 31
	s_lshl_b64 s[0:1], s[0:1], 12
	v_mfma_f32_32x32x16_f16 v[2:17], v[46:49], v[42:45], v[2:17]
	s_nop 7
	s_nop 4
	v_cvt_pk_f16_f32 v254, v2, v3
	v_cvt_pk_f16_f32 v255, v4, v5
	ds_write_b64 v251, v[254:255] offset:0
	v_cvt_pk_f16_f32 v252, v6, v7
	v_cvt_pk_f16_f32 v253, v8, v9
	ds_write_b64 v251, v[252:253] offset:16
	v_cvt_pk_f16_f32 v254, v10, v11
	v_cvt_pk_f16_f32 v255, v12, v13
	ds_write_b64 v251, v[254:255] offset:32
	v_cvt_pk_f16_f32 v252, v14, v15
	v_cvt_pk_f16_f32 v253, v16, v17
	ds_write_b64 v251, v[252:253] offset:48
	v_cvt_pk_f16_f32 v254, v18, v19
	v_cvt_pk_f16_f32 v255, v20, v21
	ds_write_b64 v251, v[254:255] offset:4608
	v_pk_add_f32 v[222:223], v[2:3], v[18:19]
	v_pk_mul_f32 v[194:195], v[2:3], v[2:3]
	v_pk_fma_f32 v[194:195], v[18:19], v[18:19], v[194:195]
	v_pk_add_f32 v[220:221], v[4:5], v[20:21]
	v_pk_mul_f32 v[192:193], v[4:5], v[4:5]
	v_pk_fma_f32 v[192:193], v[20:21], v[20:21], v[192:193]
	v_cvt_pk_f16_f32 v252, v22, v23
	v_cvt_pk_f16_f32 v253, v24, v25
	ds_write_b64 v251, v[252:253] offset:4624
	v_pk_add_f32 v[218:219], v[6:7], v[22:23]
	v_pk_mul_f32 v[184:185], v[6:7], v[6:7]
	v_pk_fma_f32 v[184:185], v[22:23], v[22:23], v[184:185]
	v_pk_add_f32 v[216:217], v[8:9], v[24:25]
	v_pk_mul_f32 v[166:167], v[8:9], v[8:9]
	v_pk_fma_f32 v[166:167], v[24:25], v[24:25], v[166:167]
	v_cvt_pk_f16_f32 v254, v26, v27
	v_cvt_pk_f16_f32 v255, v28, v29
	ds_write_b64 v251, v[254:255] offset:4640
	v_pk_add_f32 v[214:215], v[10:11], v[26:27]
	v_pk_mul_f32 v[164:165], v[10:11], v[10:11]
	v_pk_fma_f32 v[164:165], v[26:27], v[26:27], v[164:165]
	v_pk_add_f32 v[204:205], v[12:13], v[28:29]
	v_pk_mul_f32 v[162:163], v[12:13], v[12:13]
	v_pk_fma_f32 v[162:163], v[28:29], v[28:29], v[162:163]
	v_cvt_pk_f16_f32 v252, v30, v31
	v_cvt_pk_f16_f32 v253, v32, v33
	ds_write_b64 v251, v[252:253] offset:4656
	v_pk_add_f32 v[202:203], v[14:15], v[30:31]
	v_pk_mul_f32 v[160:161], v[14:15], v[14:15]
	v_pk_fma_f32 v[160:161], v[30:31], v[30:31], v[160:161]
	v_pk_add_f32 v[196:197], v[16:17], v[32:33]
	v_pk_mul_f32 v[156:157], v[16:17], v[16:17]
	v_pk_fma_f32 v[156:157], v[32:33], v[32:33], v[156:157]
	s_nop 3
	s_nop 0
	s_waitcnt lgkmcnt(0)
	s_barrier
	s_nop 4
	ds_read_b128 v[2:5], v159 offset:34816
	ds_read_b128 v[18:21], v159 offset:43520
	ds_read_b128 v[140:143], v159 offset:34848
	ds_read_b128 v[144:147], v159 offset:43552
	s_waitcnt lgkmcnt(3)
	v_mfma_f32_32x32x16_f16 v[50:65], v[2:5], v[126:129], 0
	s_add_u32 s0, s8, s0
	s_addc_u32 s1, s9, s1
	s_waitcnt lgkmcnt(2)
	v_mfma_f32_32x32x16_f16 v[34:49], v[18:21], v[126:129], 0
	v_mfma_f32_32x32x16_f16 v[2:17], v[122:125], v[2:5], v[168:183]
	v_mfma_f32_32x32x16_f16 v[18:33], v[122:125], v[18:21], v[168:183]
	ds_read_b128 v[242:245], v159 offset:34880
	ds_read_b128 v[246:249], v159 offset:43584
	s_waitcnt lgkmcnt(3)
	v_mfma_f32_32x32x16_f16 v[50:65], v[140:143], v[118:121], v[50:65]
	s_waitcnt lgkmcnt(2)
	v_mfma_f32_32x32x16_f16 v[34:49], v[144:147], v[118:121], v[34:49]
	v_mfma_f32_32x32x16_f16 v[2:17], v[114:117], v[140:143], v[2:17]
	v_mfma_f32_32x32x16_f16 v[18:33], v[114:117], v[144:147], v[18:33]
	ds_read_b128 v[140:143], v159 offset:34912
	ds_read_b128 v[144:147], v159 offset:43616
	s_waitcnt lgkmcnt(3)
	v_mfma_f32_32x32x16_f16 v[50:65], v[242:245], v[110:113], v[50:65]
	s_waitcnt lgkmcnt(2)
	v_mfma_f32_32x32x16_f16 v[34:49], v[246:249], v[110:113], v[34:49]
	v_mfma_f32_32x32x16_f16 v[2:17], v[106:109], v[242:245], v[2:17]
	v_mfma_f32_32x32x16_f16 v[18:33], v[106:109], v[246:249], v[18:33]
	ds_read_b128 v[242:245], v159 offset:34944
	ds_read_b128 v[246:249], v159 offset:43648
	s_waitcnt lgkmcnt(3)
	v_mfma_f32_32x32x16_f16 v[50:65], v[140:143], v[102:105], v[50:65]
	s_waitcnt lgkmcnt(2)
	v_mfma_f32_32x32x16_f16 v[34:49], v[144:147], v[102:105], v[34:49]
	v_mfma_f32_32x32x16_f16 v[2:17], v[98:101], v[140:143], v[2:17]
	v_mfma_f32_32x32x16_f16 v[18:33], v[98:101], v[144:147], v[18:33]
	ds_read_b128 v[186:189], v159 offset:34976
	ds_read_b128 v[206:209], v159 offset:43680
	s_waitcnt lgkmcnt(3)
	v_mfma_f32_32x32x16_f16 v[50:65], v[242:245], v[94:97], v[50:65]
	s_waitcnt lgkmcnt(2)
	v_mfma_f32_32x32x16_f16 v[34:49], v[246:249], v[94:97], v[34:49]
	v_mfma_f32_32x32x16_f16 v[2:17], v[86:89], v[242:245], v[2:17]
	v_mfma_f32_32x32x16_f16 v[18:33], v[86:89], v[246:249], v[18:33]
	ds_read_b128 v[140:143], v159 offset:35008
	ds_read_b128 v[144:147], v159 offset:43712
	s_waitcnt lgkmcnt(3)
	v_mfma_f32_32x32x16_f16 v[50:65], v[186:189], v[90:93], v[50:65]
	s_waitcnt lgkmcnt(2)
	v_mfma_f32_32x32x16_f16 v[34:49], v[206:209], v[90:93], v[34:49]
	v_mfma_f32_32x32x16_f16 v[2:17], v[78:81], v[186:189], v[2:17]
	v_mfma_f32_32x32x16_f16 v[18:33], v[78:81], v[206:209], v[18:33]
	ds_read_b128 v[186:189], v159 offset:35040
	ds_read_b128 v[206:209], v159 offset:43744
	s_waitcnt lgkmcnt(3)
	v_mfma_f32_32x32x16_f16 v[50:65], v[140:143], v[82:85], v[50:65]
	s_waitcnt lgkmcnt(2)
	v_mfma_f32_32x32x16_f16 v[34:49], v[144:147], v[82:85], v[34:49]
	v_mfma_f32_32x32x16_f16 v[2:17], v[70:73], v[140:143], v[2:17]
	v_lshlrev_b32_e32 v140, 3, v148
	v_and_b32_e32 v199, 0x1f8, v140
	global_load_dwordx2 v[148:149], v199, s[0:1]
	global_load_dwordx2 v[142:143], v199, s[0:1] offset:1024
	global_load_dwordx2 v[140:141], v199, s[0:1] offset:1536
	v_mfma_f32_32x32x16_f16 v[18:33], v[70:73], v[144:147], v[18:33]
	global_load_dwordx2 v[144:145], v199, s[0:1] offset:512
	global_load_dwordx2 v[146:147], v199, s[0:1] offset:2048
	s_waitcnt lgkmcnt(1)
	v_mfma_f32_32x32x16_f16 v[50:65], v[186:189], v[74:77], v[50:65]
	v_mfma_f32_32x32x16_f16 v[2:17], v[66:69], v[186:189], v[2:17]
	s_nop 10
	v_cvt_pk_f16_f32 v57, v56, v57
	v_cvt_pk_f16_f32 v56, v54, v55
	v_cvt_pk_f16_f32 v54, v50, v51
	s_waitcnt vmcnt(12)
	v_cvt_pk_f16_f32 v55, v52, v53
	s_waitcnt vmcnt(8)
	v_perm_b32 v50, v240, v138, s42
	v_perm_b32 v51, v240, v138, s43
	v_perm_b32 v52, v240, v139, s42
	v_perm_b32 v53, v240, v139, s43
	v_perm_b32 v139, v240, v136, s43
	v_pk_add_f16 v50, v50, s3 op_sel_hi:[1,0]
	v_pk_add_f16 v51, v51, s3 op_sel_hi:[1,0]
	v_pk_add_f16 v52, v52, s3 op_sel_hi:[1,0]
	v_pk_add_f16 v53, v53, s3 op_sel_hi:[1,0]
	v_perm_b32 v190, v240, v137, s42
	s_waitcnt lgkmcnt(0)
	v_mfma_f32_32x32x16_f16 v[18:33], v[66:69], v[206:209], v[18:33]
	v_perm_b32 v138, v240, v136, s42
	v_perm_b32 v191, v240, v137, s43
	v_pk_add_f16 v136, v138, s3 op_sel_hi:[1,0]
	v_pk_add_f16 v137, v139, s3 op_sel_hi:[1,0]
	v_pk_add_f16 v138, v190, s3 op_sel_hi:[1,0]
	v_pk_add_f16 v139, v191, s3 op_sel_hi:[1,0]
	v_cvt_pk_f16_f32 v65, v64, v65
	v_cvt_pk_f16_f32 v64, v62, v63
	v_cvt_pk_f16_f32 v63, v60, v61
	v_cvt_pk_f16_f32 v62, v58, v59
	v_mfma_f32_32x32x16_f16 v[34:49], v[206:209], v[74:77], v[34:49]
	v_mfma_f32_32x32x16_f16 v[2:17], v[54:57], v[50:53], v[2:17]
	s_waitcnt vmcnt(7)
	v_perm_b32 v58, v240, v134, s42
	v_perm_b32 v59, v240, v134, s43
	v_perm_b32 v60, v240, v135, s42
	v_perm_b32 v61, v240, v135, s43
	v_pk_add_f16 v58, v58, s3 op_sel_hi:[1,0]
	v_pk_add_f16 v59, v59, s3 op_sel_hi:[1,0]
	v_pk_add_f16 v60, v60, s3 op_sel_hi:[1,0]
	v_pk_add_f16 v61, v61, s3 op_sel_hi:[1,0]
	v_mfma_f32_32x32x16_f16 v[18:33], v[54:57], v[136:139], v[18:33]
	v_perm_b32 v134, v240, v154, s42
	v_perm_b32 v135, v240, v154, s43
	v_perm_b32 v154, v240, v155, s42
	v_perm_b32 v155, v240, v155, s43
	v_pk_add_f16 v210, v134, s3 op_sel_hi:[1,0]
	v_pk_add_f16 v211, v135, s3 op_sel_hi:[1,0]
	v_pk_add_f16 v212, v154, s3 op_sel_hi:[1,0]
	v_pk_add_f16 v213, v155, s3 op_sel_hi:[1,0]
	v_cvt_pk_f16_f32 v41, v40, v41
	v_cvt_pk_f16_f32 v40, v38, v39
	v_cvt_pk_f16_f32 v39, v36, v37
	v_cvt_pk_f16_f32 v38, v34, v35
	v_mfma_f32_32x32x16_f16 v[2:17], v[62:65], v[58:61], v[2:17]
	v_perm_b32 v34, v240, v132, s42
	v_perm_b32 v35, v240, v132, s43
	v_perm_b32 v36, v240, v133, s42
	v_perm_b32 v37, v240, v133, s43
	v_pk_add_f16 v34, v34, s3 op_sel_hi:[1,0]
	v_pk_add_f16 v35, v35, s3 op_sel_hi:[1,0]
	v_pk_add_f16 v36, v36, s3 op_sel_hi:[1,0]
	v_pk_add_f16 v37, v37, s3 op_sel_hi:[1,0]
	s_waitcnt vmcnt(6)
	v_mfma_f32_32x32x16_f16 v[18:33], v[62:65], v[210:213], v[18:33]
	v_perm_b32 v132, v240, v152, s42
	v_perm_b32 v133, v240, v152, s43
	v_perm_b32 v134, v240, v153, s42
	v_perm_b32 v53, v240, v153, s43
	v_pk_add_f16 v50, v132, s3 op_sel_hi:[1,0]
	v_pk_add_f16 v51, v133, s3 op_sel_hi:[1,0]
	v_pk_add_f16 v52, v134, s3 op_sel_hi:[1,0]
	v_pk_add_f16 v53, v53, s3 op_sel_hi:[1,0]
	v_cvt_pk_f16_f32 v49, v48, v49
	v_cvt_pk_f16_f32 v48, v46, v47
	v_cvt_pk_f16_f32 v47, v44, v45
	v_cvt_pk_f16_f32 v46, v42, v43
	v_mfma_f32_32x32x16_f16 v[2:17], v[38:41], v[34:37], v[2:17]
	v_perm_b32 v42, v240, v130, s42
	v_perm_b32 v43, v240, v130, s43
	v_perm_b32 v44, v240, v131, s42
	v_perm_b32 v45, v240, v131, s43
	v_pk_add_f16 v42, v42, s3 op_sel_hi:[1,0]
	v_pk_add_f16 v43, v43, s3 op_sel_hi:[1,0]
	v_pk_add_f16 v44, v44, s3 op_sel_hi:[1,0]
	v_pk_add_f16 v45, v45, s3 op_sel_hi:[1,0]
	s_waitcnt vmcnt(5)
	v_mfma_f32_32x32x16_f16 v[18:33], v[38:41], v[50:53], v[18:33]
	v_perm_b32 v34, v240, v150, s42
	v_perm_b32 v35, v240, v150, s43
	v_perm_b32 v36, v240, v151, s42
	v_perm_b32 v37, v240, v151, s43
	v_pk_add_f16 v34, v34, s3 op_sel_hi:[1,0]
	v_pk_add_f16 v35, v35, s3 op_sel_hi:[1,0]
	v_pk_add_f16 v36, v36, s3 op_sel_hi:[1,0]
	v_pk_add_f16 v37, v37, s3 op_sel_hi:[1,0]
	v_mfma_f32_32x32x16_f16 v[2:17], v[46:49], v[42:45], v[2:17]
	global_load_dwordx2 v[154:155], v199, s[0:1] offset:2560
	global_load_dwordx2 v[152:153], v199, s[0:1] offset:3072
	global_load_dwordx2 v[150:151], v199, s[0:1] offset:3584
	s_or_b32 s0, s10, 6
	s_ashr_i32 s1, s0, 31
	s_lshl_b64 s[0:1], s[0:1], 12
	s_add_u32 s0, s8, s0
	v_mfma_f32_32x32x16_f16 v[18:33], v[46:49], v[34:37], v[18:33]
	s_nop 7
	s_nop 4
	v_cvt_pk_f16_f32 v254, v2, v3
	v_cvt_pk_f16_f32 v255, v4, v5
	ds_write_b64 v251, v[254:255] offset:18432
	v_pk_add_f32 v[222:223], v[222:223], v[2:3]
	v_pk_fma_f32 v[194:195], v[2:3], v[2:3], v[194:195]
	v_pk_add_f32 v[220:221], v[220:221], v[4:5]
	v_pk_fma_f32 v[192:193], v[4:5], v[4:5], v[192:193]
	v_cvt_pk_f16_f32 v252, v6, v7
	v_cvt_pk_f16_f32 v253, v8, v9
	ds_write_b64 v251, v[252:253] offset:18448
	v_pk_add_f32 v[218:219], v[218:219], v[6:7]
	v_pk_fma_f32 v[184:185], v[6:7], v[6:7], v[184:185]
	v_pk_add_f32 v[216:217], v[216:217], v[8:9]
	v_pk_fma_f32 v[166:167], v[8:9], v[8:9], v[166:167]
	v_cvt_pk_f16_f32 v254, v10, v11
	v_cvt_pk_f16_f32 v255, v12, v13
	ds_write_b64 v251, v[254:255] offset:18464
	v_pk_add_f32 v[214:215], v[214:215], v[10:11]
	v_pk_fma_f32 v[164:165], v[10:11], v[10:11], v[164:165]
	v_pk_add_f32 v[204:205], v[204:205], v[12:13]
	v_pk_fma_f32 v[162:163], v[12:13], v[12:13], v[162:163]
	v_cvt_pk_f16_f32 v252, v14, v15
	v_cvt_pk_f16_f32 v253, v16, v17
	ds_write_b64 v251, v[252:253] offset:18480
	v_pk_add_f32 v[202:203], v[202:203], v[14:15]
	v_pk_fma_f32 v[160:161], v[14:15], v[14:15], v[160:161]
	v_pk_add_f32 v[196:197], v[196:197], v[16:17]
	v_pk_fma_f32 v[156:157], v[16:17], v[16:17], v[156:157]
	v_cvt_pk_f16_f32 v254, v18, v19
	v_cvt_pk_f16_f32 v255, v20, v21
	ds_write_b64 v251, v[254:255] offset:23040
	v_pk_add_f32 v[222:223], v[222:223], v[18:19]
	v_pk_fma_f32 v[194:195], v[18:19], v[18:19], v[194:195]
	v_pk_add_f32 v[220:221], v[220:221], v[20:21]
	v_pk_fma_f32 v[192:193], v[20:21], v[20:21], v[192:193]
	v_cvt_pk_f16_f32 v252, v22, v23
	v_cvt_pk_f16_f32 v253, v24, v25
	ds_write_b64 v251, v[252:253] offset:23056
	v_pk_add_f32 v[218:219], v[218:219], v[22:23]
	v_pk_fma_f32 v[184:185], v[22:23], v[22:23], v[184:185]
	v_pk_add_f32 v[216:217], v[216:217], v[24:25]
	v_pk_fma_f32 v[166:167], v[24:25], v[24:25], v[166:167]
	v_cvt_pk_f16_f32 v254, v26, v27
	v_cvt_pk_f16_f32 v255, v28, v29
	ds_write_b64 v251, v[254:255] offset:23072
	v_pk_add_f32 v[214:215], v[214:215], v[26:27]
	v_pk_fma_f32 v[164:165], v[26:27], v[26:27], v[164:165]
	v_pk_add_f32 v[204:205], v[204:205], v[28:29]
	v_pk_fma_f32 v[162:163], v[28:29], v[28:29], v[162:163]
	v_cvt_pk_f16_f32 v252, v30, v31
	v_cvt_pk_f16_f32 v253, v32, v33
	ds_write_b64 v251, v[252:253] offset:23088
	v_pk_add_f32 v[202:203], v[202:203], v[30:31]
	v_pk_fma_f32 v[160:161], v[30:31], v[30:31], v[160:161]
	v_pk_add_f32 v[196:197], v[196:197], v[32:33]
	v_pk_fma_f32 v[156:157], v[32:33], v[32:33], v[156:157]
	s_nop 3
	s_nop 0
	s_nop 0
	s_waitcnt lgkmcnt(0)
	s_barrier
	ds_read_b128 v[2:5], v159
	s_nop 2
	ds_read_b128 v[18:21], v159 offset:8704
	s_waitcnt lgkmcnt(1)
	v_mfma_f32_32x32x16_f16 v[50:65], v[2:5], v[126:129], 0
	v_lshlrev_b32_e32 v0, 3, v0
	s_addc_u32 s1, s9, s1
	v_and_b32_e32 v0, 0x1f8, v0
	global_load_dwordx2 v[138:139], v0, s[0:1]
	s_waitcnt lgkmcnt(0)
	v_mfma_f32_32x32x16_f16 v[34:49], v[18:21], v[126:129], 0
	v_mfma_f32_32x32x16_f16 v[2:17], v[122:125], v[2:5], v[168:183]
	v_mfma_f32_32x32x16_f16 v[18:33], v[122:125], v[18:21], v[168:183]
	ds_read_b128 v[130:133], v159 offset:32
	ds_read_b128 v[134:137], v159 offset:8736
	s_waitcnt lgkmcnt(1)
	v_mfma_f32_32x32x16_f16 v[50:65], v[130:133], v[118:121], v[50:65]
	s_waitcnt lgkmcnt(0)
	v_mfma_f32_32x32x16_f16 v[34:49], v[134:137], v[118:121], v[34:49]
	v_mfma_f32_32x32x16_f16 v[2:17], v[114:117], v[130:133], v[2:17]
	v_mfma_f32_32x32x16_f16 v[18:33], v[114:117], v[134:137], v[18:33]
	ds_read_b128 v[224:227], v159 offset:64
	ds_read_b128 v[228:231], v159 offset:8768
	ds_read_b128 v[130:133], v159 offset:96
	ds_read_b128 v[134:137], v159 offset:8800
	s_waitcnt lgkmcnt(3)
	v_mfma_f32_32x32x16_f16 v[50:65], v[224:227], v[110:113], v[50:65]
	s_waitcnt lgkmcnt(2)
	v_mfma_f32_32x32x16_f16 v[34:49], v[228:231], v[110:113], v[34:49]
	v_mfma_f32_32x32x16_f16 v[2:17], v[106:109], v[224:227], v[2:17]
	v_mfma_f32_32x32x16_f16 v[18:33], v[106:109], v[228:231], v[18:33]
	ds_read_b128 v[224:227], v159 offset:128
	ds_read_b128 v[228:231], v159 offset:8832
	s_waitcnt lgkmcnt(3)
	v_mfma_f32_32x32x16_f16 v[50:65], v[130:133], v[102:105], v[50:65]
	s_waitcnt lgkmcnt(2)
	v_mfma_f32_32x32x16_f16 v[34:49], v[134:137], v[102:105], v[34:49]
	v_mfma_f32_32x32x16_f16 v[2:17], v[98:101], v[130:133], v[2:17]
	v_mfma_f32_32x32x16_f16 v[18:33], v[98:101], v[134:137], v[18:33]
	ds_read_b128 v[130:133], v159 offset:160
	ds_read_b128 v[134:137], v159 offset:8864
	s_waitcnt lgkmcnt(3)
	v_mfma_f32_32x32x16_f16 v[50:65], v[224:227], v[94:97], v[50:65]
	s_waitcnt lgkmcnt(2)
	v_mfma_f32_32x32x16_f16 v[34:49], v[228:231], v[94:97], v[34:49]
	v_mfma_f32_32x32x16_f16 v[2:17], v[86:89], v[224:227], v[2:17]
	v_mfma_f32_32x32x16_f16 v[18:33], v[86:89], v[228:231], v[18:33]
	ds_read_b128 v[224:227], v159 offset:192
	ds_read_b128 v[228:231], v159 offset:8896
	s_waitcnt lgkmcnt(3)
	v_mfma_f32_32x32x16_f16 v[50:65], v[130:133], v[90:93], v[50:65]
	s_waitcnt lgkmcnt(2)
	v_mfma_f32_32x32x16_f16 v[34:49], v[134:137], v[90:93], v[34:49]
	v_mfma_f32_32x32x16_f16 v[2:17], v[78:81], v[130:133], v[2:17]
	v_mfma_f32_32x32x16_f16 v[18:33], v[78:81], v[134:137], v[18:33]
	ds_read_b128 v[232:235], v159 offset:224
	ds_read_b128 v[236:239], v159 offset:8928
	s_waitcnt lgkmcnt(3)
	v_mfma_f32_32x32x16_f16 v[50:65], v[224:227], v[82:85], v[50:65]
	global_load_dwordx2 v[134:135], v0, s[0:1] offset:512
	global_load_dwordx2 v[132:133], v0, s[0:1] offset:1024
	global_load_dwordx2 v[130:131], v0, s[0:1] offset:1536
	s_waitcnt lgkmcnt(2)
	v_mfma_f32_32x32x16_f16 v[34:49], v[228:231], v[82:85], v[34:49]
	global_load_dwordx2 v[136:137], v0, s[0:1] offset:2048
	v_mfma_f32_32x32x16_f16 v[2:17], v[70:73], v[224:227], v[2:17]
	v_mfma_f32_32x32x16_f16 v[18:33], v[70:73], v[228:231], v[18:33]
	s_waitcnt lgkmcnt(1)
	v_mfma_f32_32x32x16_f16 v[50:65], v[232:235], v[74:77], v[50:65]
	v_mfma_f32_32x32x16_f16 v[2:17], v[66:69], v[232:235], v[2:17]
	s_nop 10
	v_cvt_pk_f16_f32 v57, v56, v57
	v_cvt_pk_f16_f32 v56, v54, v55
	v_cvt_pk_f16_f32 v54, v50, v51
	s_waitcnt vmcnt(12)
	v_lshlrev_b32_e32 v50, 8, v148
	v_cvt_pk_f16_f32 v55, v52, v53
	v_perm_b32 v50, v50, v148, s2
	v_lshrrev_b32_e32 v51, 16, v148
	v_lshrrev_b32_e32 v52, 8, v148
	v_lshrrev_b32_e32 v53, 16, v149
	v_lshrrev_b32_e32 v148, 8, v149
	v_perm_b32 v51, v52, v51, s2
	v_lshlrev_b32_e32 v52, 8, v149
	v_perm_b32 v53, v148, v53, s2
	s_waitcnt vmcnt(8)
	v_perm_b32 v52, v52, v149, s2
	v_perm_b32 v149, v240, v146, s43
	v_perm_b32 v198, v240, v147, s42
	s_waitcnt lgkmcnt(0)
	v_mfma_f32_32x32x16_f16 v[18:33], v[66:69], v[236:239], v[18:33]
	v_or_b32_e32 v50, 0x64006400, v50
	v_or_b32_e32 v51, 0x64006400, v51
	v_or_b32_e32 v52, 0x64006400, v52
	v_or_b32_e32 v53, 0x64006400, v53
	v_pk_add_f16 v50, v50, s3 op_sel_hi:[1,0]
	v_pk_add_f16 v51, v51, s3 op_sel_hi:[1,0]
	v_pk_add_f16 v52, v52, s3 op_sel_hi:[1,0]
	v_pk_add_f16 v53, v53, s3 op_sel_hi:[1,0]
	v_perm_b32 v148, v240, v146, s42
	v_perm_b32 v200, v240, v147, s43
	v_pk_add_f16 v146, v148, s3 op_sel_hi:[1,0]
	v_pk_add_f16 v147, v149, s3 op_sel_hi:[1,0]
	v_pk_add_f16 v148, v198, s3 op_sel_hi:[1,0]
	v_pk_add_f16 v149, v200, s3 op_sel_hi:[1,0]
	v_cvt_pk_f16_f32 v65, v64, v65
	v_cvt_pk_f16_f32 v64, v62, v63
	v_cvt_pk_f16_f32 v62, v58, v59
	v_cvt_pk_f16_f32 v63, v60, v61
	s_waitcnt vmcnt(7)
	v_mfma_f32_32x32x16_f16 v[34:49], v[236:239], v[74:77], v[34:49]
	v_mfma_f32_32x32x16_f16 v[2:17], v[54:57], v[50:53], v[2:17]
	v_perm_b32 v58, v240, v144, s42
	v_perm_b32 v59, v240, v144, s43
	v_perm_b32 v60, v240, v145, s42
	v_perm_b32 v61, v240, v145, s43
	v_mfma_f32_32x32x16_f16 v[18:33], v[54:57], v[146:149], v[18:33]
	v_pk_add_f16 v58, v58, s3 op_sel_hi:[1,0]
	v_pk_add_f16 v59, v59, s3 op_sel_hi:[1,0]
	v_pk_add_f16 v60, v60, s3 op_sel_hi:[1,0]
	v_pk_add_f16 v61, v61, s3 op_sel_hi:[1,0]
	v_perm_b32 v144, v240, v154, s42
	v_perm_b32 v145, v240, v154, s43
	v_perm_b32 v154, v240, v155, s42
	v_perm_b32 v155, v240, v155, s43
	v_pk_add_f16 v224, v144, s3 op_sel_hi:[1,0]
	v_pk_add_f16 v225, v145, s3 op_sel_hi:[1,0]
	v_pk_add_f16 v226, v154, s3 op_sel_hi:[1,0]
	v_pk_add_f16 v227, v155, s3 op_sel_hi:[1,0]
	v_cvt_pk_f16_f32 v41, v40, v41
	v_cvt_pk_f16_f32 v40, v38, v39
	v_cvt_pk_f16_f32 v39, v36, v37
	v_cvt_pk_f16_f32 v38, v34, v35
	s_waitcnt vmcnt(6)
	v_mfma_f32_32x32x16_f16 v[2:17], v[62:65], v[58:61], v[2:17]
	v_perm_b32 v34, v240, v142, s42
	v_perm_b32 v35, v240, v142, s43
	v_mfma_f32_32x32x16_f16 v[18:33], v[62:65], v[224:227], v[18:33]
	v_perm_b32 v36, v240, v143, s42
	v_perm_b32 v37, v240, v143, s43
	v_pk_add_f16 v34, v34, s3 op_sel_hi:[1,0]
	v_pk_add_f16 v35, v35, s3 op_sel_hi:[1,0]
	v_pk_add_f16 v36, v36, s3 op_sel_hi:[1,0]
	v_pk_add_f16 v37, v37, s3 op_sel_hi:[1,0]
	v_perm_b32 v142, v240, v152, s42
	v_perm_b32 v143, v240, v152, s43
	v_perm_b32 v144, v240, v153, s42
	v_perm_b32 v53, v240, v153, s43
	v_pk_add_f16 v50, v142, s3 op_sel_hi:[1,0]
	v_pk_add_f16 v51, v143, s3 op_sel_hi:[1,0]
	v_pk_add_f16 v52, v144, s3 op_sel_hi:[1,0]
	v_pk_add_f16 v53, v53, s3 op_sel_hi:[1,0]
	v_cvt_pk_f16_f32 v49, v48, v49
	v_cvt_pk_f16_f32 v48, v46, v47
	v_cvt_pk_f16_f32 v47, v44, v45
	v_cvt_pk_f16_f32 v46, v42, v43
	v_mfma_f32_32x32x16_f16 v[2:17], v[38:41], v[34:37], v[2:17]
	s_waitcnt vmcnt(5)
	v_mfma_f32_32x32x16_f16 v[18:33], v[38:41], v[50:53], v[18:33]
	v_perm_b32 v42, v240, v140, s42
	v_perm_b32 v43, v240, v140, s43
	v_perm_b32 v44, v240, v141, s42
	v_perm_b32 v45, v240, v141, s43
	v_perm_b32 v34, v240, v150, s42
	v_perm_b32 v35, v240, v150, s43
	v_perm_b32 v36, v240, v151, s42
	v_perm_b32 v37, v240, v151, s43
	v_pk_add_f16 v42, v42, s3 op_sel_hi:[1,0]
	v_pk_add_f16 v43, v43, s3 op_sel_hi:[1,0]
	v_pk_add_f16 v44, v44, s3 op_sel_hi:[1,0]
	v_pk_add_f16 v45, v45, s3 op_sel_hi:[1,0]
	v_pk_add_f16 v34, v34, s3 op_sel_hi:[1,0]
	v_pk_add_f16 v35, v35, s3 op_sel_hi:[1,0]
	v_pk_add_f16 v36, v36, s3 op_sel_hi:[1,0]
	v_pk_add_f16 v37, v37, s3 op_sel_hi:[1,0]
	v_mfma_f32_32x32x16_f16 v[2:17], v[46:49], v[42:45], v[2:17]
	global_load_dwordx2 v[142:143], v0, s[0:1] offset:2560
	global_load_dwordx2 v[140:141], v0, s[0:1] offset:3072
	global_load_dwordx2 v[64:65], v0, s[0:1] offset:3584
	v_mfma_f32_32x32x16_f16 v[18:33], v[46:49], v[34:37], v[18:33]
	s_nop 7
	s_nop 4
	v_cvt_pk_f16_f32 v254, v2, v3
	v_cvt_pk_f16_f32 v255, v4, v5
	ds_write_b64 v251, v[254:255] offset:0
	v_pk_add_f32 v[222:223], v[222:223], v[2:3]
	v_pk_fma_f32 v[194:195], v[2:3], v[2:3], v[194:195]
	v_pk_add_f32 v[220:221], v[220:221], v[4:5]
	v_pk_fma_f32 v[192:193], v[4:5], v[4:5], v[192:193]
	v_cvt_pk_f16_f32 v252, v6, v7
	v_cvt_pk_f16_f32 v253, v8, v9
	ds_write_b64 v251, v[252:253] offset:16
	v_pk_add_f32 v[218:219], v[218:219], v[6:7]
	v_pk_fma_f32 v[184:185], v[6:7], v[6:7], v[184:185]
	v_pk_add_f32 v[216:217], v[216:217], v[8:9]
	v_pk_fma_f32 v[166:167], v[8:9], v[8:9], v[166:167]
	v_cvt_pk_f16_f32 v254, v10, v11
	v_cvt_pk_f16_f32 v255, v12, v13
	ds_write_b64 v251, v[254:255] offset:32
	v_pk_add_f32 v[214:215], v[214:215], v[10:11]
	v_pk_fma_f32 v[164:165], v[10:11], v[10:11], v[164:165]
	v_pk_add_f32 v[204:205], v[204:205], v[12:13]
	v_pk_fma_f32 v[162:163], v[12:13], v[12:13], v[162:163]
	v_cvt_pk_f16_f32 v252, v14, v15
	v_cvt_pk_f16_f32 v253, v16, v17
	ds_write_b64 v251, v[252:253] offset:48
	v_pk_add_f32 v[202:203], v[202:203], v[14:15]
	v_pk_fma_f32 v[160:161], v[14:15], v[14:15], v[160:161]
	v_pk_add_f32 v[196:197], v[196:197], v[16:17]
	v_pk_fma_f32 v[156:157], v[16:17], v[16:17], v[156:157]
	v_cvt_pk_f16_f32 v254, v18, v19
	v_cvt_pk_f16_f32 v255, v20, v21
	ds_write_b64 v251, v[254:255] offset:4608
	v_pk_add_f32 v[222:223], v[222:223], v[18:19]
	v_pk_fma_f32 v[194:195], v[18:19], v[18:19], v[194:195]
	v_pk_add_f32 v[220:221], v[220:221], v[20:21]
	v_pk_fma_f32 v[192:193], v[20:21], v[20:21], v[192:193]
	v_cvt_pk_f16_f32 v252, v22, v23
	v_cvt_pk_f16_f32 v253, v24, v25
	ds_write_b64 v251, v[252:253] offset:4624
	v_pk_add_f32 v[218:219], v[218:219], v[22:23]
	v_pk_fma_f32 v[184:185], v[22:23], v[22:23], v[184:185]
	v_pk_add_f32 v[216:217], v[216:217], v[24:25]
	v_pk_fma_f32 v[166:167], v[24:25], v[24:25], v[166:167]
	v_cvt_pk_f16_f32 v254, v26, v27
	v_cvt_pk_f16_f32 v255, v28, v29
	ds_write_b64 v251, v[254:255] offset:4640
	v_pk_add_f32 v[214:215], v[214:215], v[26:27]
	v_pk_fma_f32 v[164:165], v[26:27], v[26:27], v[164:165]
	v_pk_add_f32 v[204:205], v[204:205], v[28:29]
	v_pk_fma_f32 v[162:163], v[28:29], v[28:29], v[162:163]
	v_cvt_pk_f16_f32 v252, v30, v31
	v_cvt_pk_f16_f32 v253, v32, v33
	ds_write_b64 v251, v[252:253] offset:4656
	v_pk_add_f32 v[202:203], v[202:203], v[30:31]
	v_pk_fma_f32 v[160:161], v[30:31], v[30:31], v[160:161]
	v_pk_add_f32 v[196:197], v[196:197], v[32:33]
	v_pk_fma_f32 v[156:157], v[32:33], v[32:33], v[156:157]
	s_nop 7
	s_waitcnt lgkmcnt(0)
	s_barrier
	s_nop 1
	ds_read_b128 v[16:19], v159 offset:43520
	s_waitcnt lgkmcnt(0)
	v_mfma_f32_32x32x16_f16 v[32:47], v[16:19], v[126:129], 0
	ds_read_b128 v[2:5], v159 offset:34816
	s_waitcnt lgkmcnt(0)
	v_mfma_f32_32x32x16_f16 v[48:63], v[2:5], v[126:129], 0
	ds_read_b128 v[126:129], v159 offset:34848
	s_waitcnt lgkmcnt(0)
	v_mfma_f32_32x32x16_f16 v[48:63], v[126:129], v[118:121], v[48:63]
	v_mfma_f32_32x32x16_f16 v[0:15], v[122:125], v[2:5], v[168:183]
	v_mfma_f32_32x32x16_f16 v[0:15], v[114:117], v[126:129], v[0:15]
	v_mfma_f32_32x32x16_f16 v[16:31], v[122:125], v[16:19], v[168:183]
	ds_read_b128 v[122:125], v159 offset:43552
	s_waitcnt lgkmcnt(0)
	v_mfma_f32_32x32x16_f16 v[32:47], v[122:125], v[118:121], v[32:47]
	v_mfma_f32_32x32x16_f16 v[16:31], v[114:117], v[122:125], v[16:31]
	ds_read_b128 v[118:121], v159 offset:34880
	ds_read_b128 v[114:117], v159 offset:43584
	s_waitcnt lgkmcnt(1)
	v_mfma_f32_32x32x16_f16 v[48:63], v[118:121], v[110:113], v[48:63]
	s_waitcnt lgkmcnt(0)
	v_mfma_f32_32x32x16_f16 v[32:47], v[114:117], v[110:113], v[32:47]
	v_mfma_f32_32x32x16_f16 v[0:15], v[106:109], v[118:121], v[0:15]
	ds_read_b128 v[110:113], v159 offset:34912
	v_mfma_f32_32x32x16_f16 v[16:31], v[106:109], v[114:117], v[16:31]
	ds_read_b128 v[106:109], v159 offset:43616
	s_waitcnt lgkmcnt(1)
	v_mfma_f32_32x32x16_f16 v[48:63], v[110:113], v[102:105], v[48:63]
	s_waitcnt lgkmcnt(0)
	v_mfma_f32_32x32x16_f16 v[32:47], v[106:109], v[102:105], v[32:47]
	v_mfma_f32_32x32x16_f16 v[0:15], v[98:101], v[110:113], v[0:15]
	ds_read_b128 v[102:105], v159 offset:34944
	v_mfma_f32_32x32x16_f16 v[16:31], v[98:101], v[106:109], v[16:31]
	ds_read_b128 v[98:101], v159 offset:43648
	s_waitcnt lgkmcnt(1)
	v_mfma_f32_32x32x16_f16 v[48:63], v[102:105], v[94:97], v[48:63]
	s_waitcnt lgkmcnt(0)
	v_mfma_f32_32x32x16_f16 v[32:47], v[98:101], v[94:97], v[32:47]
	v_mfma_f32_32x32x16_f16 v[0:15], v[86:89], v[102:105], v[0:15]
	ds_read_b128 v[94:97], v159 offset:34976
	v_mfma_f32_32x32x16_f16 v[16:31], v[86:89], v[98:101], v[16:31]
	ds_read_b128 v[86:89], v159 offset:43680
	s_waitcnt lgkmcnt(1)
	v_mfma_f32_32x32x16_f16 v[48:63], v[94:97], v[90:93], v[48:63]
	s_waitcnt lgkmcnt(0)
	v_mfma_f32_32x32x16_f16 v[32:47], v[86:89], v[90:93], v[32:47]
	v_mfma_f32_32x32x16_f16 v[0:15], v[78:81], v[94:97], v[0:15]
	ds_read_b128 v[90:93], v159 offset:35008
	v_mfma_f32_32x32x16_f16 v[16:31], v[78:81], v[86:89], v[16:31]
	ds_read_b128 v[78:81], v159 offset:43712
	s_waitcnt lgkmcnt(1)
	v_mfma_f32_32x32x16_f16 v[48:63], v[90:93], v[82:85], v[48:63]
	s_waitcnt lgkmcnt(0)
	v_mfma_f32_32x32x16_f16 v[32:47], v[78:81], v[82:85], v[32:47]
	v_mfma_f32_32x32x16_f16 v[0:15], v[70:73], v[90:93], v[0:15]
	ds_read_b128 v[82:85], v159 offset:35040
	v_mfma_f32_32x32x16_f16 v[16:31], v[70:73], v[78:81], v[16:31]
	ds_read_b128 v[70:73], v159 offset:43744
	s_waitcnt lgkmcnt(1)
	v_mfma_f32_32x32x16_f16 v[48:63], v[82:85], v[74:77], v[48:63]
	v_mfma_f32_32x32x16_f16 v[0:15], v[66:69], v[82:85], v[0:15]
	s_nop 3
	s_nop 6
	v_cvt_pk_f16_f32 v55, v54, v55
	v_cvt_pk_f16_f32 v54, v52, v53
	v_cvt_pk_f16_f32 v53, v50, v51
	v_cvt_pk_f16_f32 v52, v48, v49
	s_waitcnt vmcnt(3)
	s_waitcnt lgkmcnt(0)
	v_mfma_f32_32x32x16_f16 v[16:31], v[66:69], v[70:73], v[16:31]
	v_lshrrev_b32_e32 v69, 16, v139
	v_mfma_f32_32x32x16_f16 v[32:47], v[70:73], v[74:77], v[32:47]
	v_lshrrev_b32_e32 v70, 8, v139
	v_perm_b32 v69, v70, v69, s2
	v_perm_b32 v66, v240, v138, s42
	v_perm_b32 v67, v240, v138, s43
	v_perm_b32 v68, v240, v139, s42
	v_or_b32_e32 v69, 0x64006400, v69
	v_pk_add_f16 v66, v66, s3 op_sel_hi:[1,0]
	v_pk_add_f16 v67, v67, s3 op_sel_hi:[1,0]
	v_pk_add_f16 v68, v68, s3 op_sel_hi:[1,0]
	v_pk_add_f16 v69, v69, s3 op_sel_hi:[1,0]
	s_nop 1
	v_mfma_f32_32x32x16_f16 v[0:15], v[52:55], v[66:69], v[0:15]
	v_perm_b32 v48, v240, v136, s42
	v_perm_b32 v49, v240, v136, s43
	v_perm_b32 v50, v240, v137, s42
	v_perm_b32 v51, v240, v137, s43
	v_pk_add_f16 v48, v48, s3 op_sel_hi:[1,0]
	v_pk_add_f16 v49, v49, s3 op_sel_hi:[1,0]
	v_pk_add_f16 v50, v50, s3 op_sel_hi:[1,0]
	v_pk_add_f16 v51, v51, s3 op_sel_hi:[1,0]
	v_cvt_pk_f16_f32 v39, v38, v39
	v_cvt_pk_f16_f32 v38, v36, v37
	v_mfma_f32_32x32x16_f16 v[16:31], v[52:55], v[48:51], v[16:31]
	v_perm_b32 v48, v240, v134, s42
	v_perm_b32 v49, v240, v134, s43
	v_perm_b32 v50, v240, v135, s42
	v_perm_b32 v51, v240, v135, s43
	v_pk_add_f16 v48, v48, s3 op_sel_hi:[1,0]
	v_pk_add_f16 v49, v49, s3 op_sel_hi:[1,0]
	v_pk_add_f16 v50, v50, s3 op_sel_hi:[1,0]
	v_pk_add_f16 v51, v51, s3 op_sel_hi:[1,0]
	v_cvt_pk_f16_f32 v55, v62, v63
	v_cvt_pk_f16_f32 v54, v60, v61
	v_cvt_pk_f16_f32 v53, v58, v59
	v_cvt_pk_f16_f32 v52, v56, v57
	s_waitcnt vmcnt(2)
	v_cvt_pk_f16_f32 v37, v34, v35
	v_mfma_f32_32x32x16_f16 v[0:15], v[52:55], v[48:51], v[0:15]
	v_perm_b32 v48, v240, v142, s42
	v_perm_b32 v49, v240, v142, s43
	v_perm_b32 v50, v240, v143, s42
	v_perm_b32 v51, v240, v143, s43
	v_pk_add_f16 v48, v48, s3 op_sel_hi:[1,0]
	v_pk_add_f16 v49, v49, s3 op_sel_hi:[1,0]
	v_pk_add_f16 v50, v50, s3 op_sel_hi:[1,0]
	v_pk_add_f16 v51, v51, s3 op_sel_hi:[1,0]
	v_cvt_pk_f16_f32 v36, v32, v33
	s_waitcnt vmcnt(1)
	v_mfma_f32_32x32x16_f16 v[16:31], v[52:55], v[48:51], v[16:31]
	v_lshrrev_b32_e32 v51, 16, v133
	v_lshrrev_b32_e32 v52, 8, v133
	v_perm_b32 v51, v52, v51, s2
	v_perm_b32 v48, v240, v132, s42
	v_perm_b32 v49, v240, v132, s43
	v_perm_b32 v50, v240, v133, s42
	v_or_b32_e32 v51, 0x64006400, v51
	v_pk_add_f16 v48, v48, s3 op_sel_hi:[1,0]
	v_pk_add_f16 v49, v49, s3 op_sel_hi:[1,0]
	v_pk_add_f16 v50, v50, s3 op_sel_hi:[1,0]
	v_pk_add_f16 v51, v51, s3 op_sel_hi:[1,0]
	s_nop 1
	v_mfma_f32_32x32x16_f16 v[0:15], v[36:39], v[48:51], v[0:15]
	v_perm_b32 v32, v240, v140, s42
	v_perm_b32 v33, v240, v140, s43
	v_perm_b32 v34, v240, v141, s42
	v_perm_b32 v35, v240, v141, s43
	v_pk_add_f16 v32, v32, s3 op_sel_hi:[1,0]
	v_pk_add_f16 v33, v33, s3 op_sel_hi:[1,0]
	v_pk_add_f16 v34, v34, s3 op_sel_hi:[1,0]
	v_pk_add_f16 v35, v35, s3 op_sel_hi:[1,0]
	s_nop 1
	v_mfma_f32_32x32x16_f16 v[16:31], v[36:39], v[32:35], v[16:31]
	v_perm_b32 v32, v240, v130, s42
	v_perm_b32 v33, v240, v130, s43
	v_perm_b32 v34, v240, v131, s42
	v_perm_b32 v35, v240, v131, s43
	v_pk_add_f16 v32, v32, s3 op_sel_hi:[1,0]
	v_pk_add_f16 v33, v33, s3 op_sel_hi:[1,0]
	v_pk_add_f16 v34, v34, s3 op_sel_hi:[1,0]
	v_pk_add_f16 v35, v35, s3 op_sel_hi:[1,0]
	v_cvt_pk_f16_f32 v39, v46, v47
	v_cvt_pk_f16_f32 v38, v44, v45
	v_cvt_pk_f16_f32 v37, v42, v43
	v_cvt_pk_f16_f32 v36, v40, v41
	s_waitcnt vmcnt(0)
	s_nop 0
	v_mfma_f32_32x32x16_f16 v[0:15], v[36:39], v[32:35], v[0:15]
	v_perm_b32 v32, v240, v64, s42
	v_perm_b32 v33, v240, v64, s43
	v_perm_b32 v34, v240, v65, s42
	v_perm_b32 v35, v240, v65, s43
	v_pk_add_f16 v32, v32, s3 op_sel_hi:[1,0]
	v_pk_add_f16 v33, v33, s3 op_sel_hi:[1,0]
	v_pk_add_f16 v34, v34, s3 op_sel_hi:[1,0]
	v_pk_add_f16 v35, v35, s3 op_sel_hi:[1,0]
	s_nop 3
	v_mfma_f32_32x32x16_f16 v[16:31], v[36:39], v[32:35], v[16:31]
	s_nop 7
	s_nop 4
	v_cvt_pk_f16_f32 v254, v0, v1
	v_cvt_pk_f16_f32 v255, v2, v3
	ds_write_b64 v251, v[254:255] offset:18432
	v_pk_add_f32 v[222:223], v[222:223], v[0:1]
	v_pk_fma_f32 v[194:195], v[0:1], v[0:1], v[194:195]
	v_pk_add_f32 v[220:221], v[220:221], v[2:3]
	v_pk_fma_f32 v[192:193], v[2:3], v[2:3], v[192:193]
	v_cvt_pk_f16_f32 v252, v4, v5
	v_cvt_pk_f16_f32 v253, v6, v7
	ds_write_b64 v251, v[252:253] offset:18448
	v_pk_add_f32 v[218:219], v[218:219], v[4:5]
	v_pk_fma_f32 v[184:185], v[4:5], v[4:5], v[184:185]
	v_pk_add_f32 v[216:217], v[216:217], v[6:7]
	v_pk_fma_f32 v[166:167], v[6:7], v[6:7], v[166:167]
	v_cvt_pk_f16_f32 v254, v8, v9
	v_cvt_pk_f16_f32 v255, v10, v11
	ds_write_b64 v251, v[254:255] offset:18464
	v_pk_add_f32 v[214:215], v[214:215], v[8:9]
	v_pk_fma_f32 v[164:165], v[8:9], v[8:9], v[164:165]
	v_pk_add_f32 v[204:205], v[204:205], v[10:11]
	v_pk_fma_f32 v[162:163], v[10:11], v[10:11], v[162:163]
	v_cvt_pk_f16_f32 v252, v12, v13
	v_cvt_pk_f16_f32 v253, v14, v15
	ds_write_b64 v251, v[252:253] offset:18480
	v_pk_add_f32 v[202:203], v[202:203], v[12:13]
	v_pk_fma_f32 v[160:161], v[12:13], v[12:13], v[160:161]
	v_pk_add_f32 v[196:197], v[196:197], v[14:15]
	v_pk_fma_f32 v[156:157], v[14:15], v[14:15], v[156:157]
	v_cvt_pk_f16_f32 v254, v16, v17
	v_cvt_pk_f16_f32 v255, v18, v19
	ds_write_b64 v251, v[254:255] offset:23040
	v_pk_add_f32 v[222:223], v[222:223], v[16:17]
	v_pk_fma_f32 v[194:195], v[16:17], v[16:17], v[194:195]
	v_pk_add_f32 v[220:221], v[220:221], v[18:19]
	v_pk_fma_f32 v[192:193], v[18:19], v[18:19], v[192:193]
	v_cvt_pk_f16_f32 v252, v20, v21
	v_cvt_pk_f16_f32 v253, v22, v23
	ds_write_b64 v251, v[252:253] offset:23056
	v_pk_add_f32 v[218:219], v[218:219], v[20:21]
	v_pk_fma_f32 v[184:185], v[20:21], v[20:21], v[184:185]
	v_pk_add_f32 v[216:217], v[216:217], v[22:23]
	v_pk_fma_f32 v[166:167], v[22:23], v[22:23], v[166:167]
	v_cvt_pk_f16_f32 v254, v24, v25
	v_cvt_pk_f16_f32 v255, v26, v27
	ds_write_b64 v251, v[254:255] offset:23072
	v_pk_add_f32 v[214:215], v[214:215], v[24:25]
	v_pk_fma_f32 v[164:165], v[24:25], v[24:25], v[164:165]
	v_pk_add_f32 v[204:205], v[204:205], v[26:27]
	v_pk_fma_f32 v[162:163], v[26:27], v[26:27], v[162:163]
	v_cvt_pk_f16_f32 v252, v28, v29
	v_cvt_pk_f16_f32 v253, v30, v31
	ds_write_b64 v251, v[252:253] offset:23088
	v_pk_add_f32 v[202:203], v[202:203], v[28:29]
	v_pk_fma_f32 v[160:161], v[28:29], v[28:29], v[160:161]
	v_pk_add_f32 v[196:197], v[196:197], v[30:31]
	v_pk_fma_f32 v[156:157], v[30:31], v[30:31], v[156:157]
	s_nop 4
	s_nop 0
	v_add_f32_dpp v222, v222, v222 row_half_mirror row_mask:0xf bank_mask:0x5
	v_add_f32_dpp v222, v223, v223 row_half_mirror row_mask:0xf bank_mask:0xa
	v_add_f32_dpp v220, v220, v220 row_half_mirror row_mask:0xf bank_mask:0x5
	v_add_f32_dpp v220, v221, v221 row_half_mirror row_mask:0xf bank_mask:0xa
	v_add_f32_dpp v218, v218, v218 row_half_mirror row_mask:0xf bank_mask:0x5
	v_add_f32_dpp v218, v219, v219 row_half_mirror row_mask:0xf bank_mask:0xa
	v_add_f32_dpp v216, v216, v216 row_half_mirror row_mask:0xf bank_mask:0x5
	v_add_f32_dpp v216, v217, v217 row_half_mirror row_mask:0xf bank_mask:0xa
	v_add_f32_dpp v214, v214, v214 row_half_mirror row_mask:0xf bank_mask:0x5
	v_add_f32_dpp v214, v215, v215 row_half_mirror row_mask:0xf bank_mask:0xa
	v_add_f32_dpp v204, v204, v204 row_half_mirror row_mask:0xf bank_mask:0x5
	v_add_f32_dpp v204, v205, v205 row_half_mirror row_mask:0xf bank_mask:0xa
	v_add_f32_dpp v202, v202, v202 row_half_mirror row_mask:0xf bank_mask:0x5
	v_add_f32_dpp v202, v203, v203 row_half_mirror row_mask:0xf bank_mask:0xa
	v_add_f32_dpp v196, v196, v196 row_half_mirror row_mask:0xf bank_mask:0x5
	v_add_f32_dpp v196, v197, v197 row_half_mirror row_mask:0xf bank_mask:0xa
	v_add_f32_dpp v194, v194, v194 row_half_mirror row_mask:0xf bank_mask:0x5
	v_add_f32_dpp v194, v195, v195 row_half_mirror row_mask:0xf bank_mask:0xa
	v_add_f32_dpp v192, v192, v192 row_half_mirror row_mask:0xf bank_mask:0x5
	v_add_f32_dpp v192, v193, v193 row_half_mirror row_mask:0xf bank_mask:0xa
	v_add_f32_dpp v184, v184, v184 row_half_mirror row_mask:0xf bank_mask:0x5
	v_add_f32_dpp v184, v185, v185 row_half_mirror row_mask:0xf bank_mask:0xa
	v_add_f32_dpp v166, v166, v166 row_half_mirror row_mask:0xf bank_mask:0x5
	v_add_f32_dpp v166, v167, v167 row_half_mirror row_mask:0xf bank_mask:0xa
	v_add_f32_dpp v164, v164, v164 row_half_mirror row_mask:0xf bank_mask:0x5
	v_add_f32_dpp v164, v165, v165 row_half_mirror row_mask:0xf bank_mask:0xa
	v_add_f32_dpp v162, v162, v162 row_half_mirror row_mask:0xf bank_mask:0x5
	v_add_f32_dpp v162, v163, v163 row_half_mirror row_mask:0xf bank_mask:0xa
	v_add_f32_dpp v160, v160, v160 row_half_mirror row_mask:0xf bank_mask:0x5
	v_add_f32_dpp v160, v161, v161 row_half_mirror row_mask:0xf bank_mask:0xa
	v_add_f32_dpp v156, v156, v156 row_half_mirror row_mask:0xf bank_mask:0x5
	v_add_f32_dpp v156, v157, v157 row_half_mirror row_mask:0xf bank_mask:0xa
	v_add_f32_dpp v222, v222, v222 row_ror:8 row_mask:0xf bank_mask:0x3
	v_add_f32_dpp v222, v220, v220 row_ror:8 row_mask:0xf bank_mask:0xc
	v_add_f32_dpp v218, v218, v218 row_ror:8 row_mask:0xf bank_mask:0x3
	v_add_f32_dpp v218, v216, v216 row_ror:8 row_mask:0xf bank_mask:0xc
	v_add_f32_dpp v214, v214, v214 row_ror:8 row_mask:0xf bank_mask:0x3
	v_add_f32_dpp v214, v204, v204 row_ror:8 row_mask:0xf bank_mask:0xc
	v_add_f32_dpp v202, v202, v202 row_ror:8 row_mask:0xf bank_mask:0x3
	v_add_f32_dpp v202, v196, v196 row_ror:8 row_mask:0xf bank_mask:0xc
	v_add_f32_dpp v194, v194, v194 row_ror:8 row_mask:0xf bank_mask:0x3
	v_add_f32_dpp v194, v192, v192 row_ror:8 row_mask:0xf bank_mask:0xc
	v_add_f32_dpp v184, v184, v184 row_ror:8 row_mask:0xf bank_mask:0x3
	v_add_f32_dpp v184, v166, v166 row_ror:8 row_mask:0xf bank_mask:0xc
	v_add_f32_dpp v164, v164, v164 row_ror:8 row_mask:0xf bank_mask:0x3
	v_add_f32_dpp v164, v162, v162 row_ror:8 row_mask:0xf bank_mask:0xc
	v_add_f32_dpp v160, v160, v160 row_ror:8 row_mask:0xf bank_mask:0x3
	v_add_f32_dpp v160, v156, v156 row_ror:8 row_mask:0xf bank_mask:0xc
	v_add_f32_dpp v222, v222, v222 quad_perm:[1,0,3,2] row_mask:0xf bank_mask:0xf
	v_add_f32_dpp v218, v218, v218 quad_perm:[1,0,3,2] row_mask:0xf bank_mask:0xf
	v_add_f32_dpp v214, v214, v214 quad_perm:[1,0,3,2] row_mask:0xf bank_mask:0xf
	v_add_f32_dpp v202, v202, v202 quad_perm:[1,0,3,2] row_mask:0xf bank_mask:0xf
	v_add_f32_dpp v194, v194, v194 quad_perm:[1,0,3,2] row_mask:0xf bank_mask:0xf
	v_add_f32_dpp v184, v184, v184 quad_perm:[1,0,3,2] row_mask:0xf bank_mask:0xf
	v_add_f32_dpp v164, v164, v164 quad_perm:[1,0,3,2] row_mask:0xf bank_mask:0xf
	v_add_f32_dpp v160, v160, v160 quad_perm:[1,0,3,2] row_mask:0xf bank_mask:0xf
	v_add_f32_dpp v222, v222, v222 quad_perm:[2,3,0,1] row_mask:0xf bank_mask:0xf
	v_add_f32_dpp v218, v218, v218 quad_perm:[2,3,0,1] row_mask:0xf bank_mask:0xf
	v_add_f32_dpp v214, v214, v214 quad_perm:[2,3,0,1] row_mask:0xf bank_mask:0xf
	v_add_f32_dpp v202, v202, v202 quad_perm:[2,3,0,1] row_mask:0xf bank_mask:0xf
	v_add_f32_dpp v194, v194, v194 quad_perm:[2,3,0,1] row_mask:0xf bank_mask:0xf
	v_add_f32_dpp v184, v184, v184 quad_perm:[2,3,0,1] row_mask:0xf bank_mask:0xf
	v_add_f32_dpp v164, v164, v164 quad_perm:[2,3,0,1] row_mask:0xf bank_mask:0xf
	v_add_f32_dpp v160, v160, v160 quad_perm:[2,3,0,1] row_mask:0xf bank_mask:0xf
	s_mov_b32 exec_lo, 0x1111
	s_mov_b32 exec_hi, 0x1111
	ds_add_f32 v250, v222 offset:0
	ds_add_f32 v250, v218 offset:32
	ds_add_f32 v250, v214 offset:64
	ds_add_f32 v250, v202 offset:96
	ds_add_f32 v250, v194 offset:256
	ds_add_f32 v250, v184 offset:288
	ds_add_f32 v250, v164 offset:320
	ds_add_f32 v250, v160 offset:352
	s_waitcnt lgkmcnt(7)
	s_mov_b32 exec_lo, 0x11110000
	s_mov_b32 exec_hi, 0x11110000
	ds_add_f32 v250, v222 offset:0
	ds_add_f32 v250, v218 offset:32
	ds_add_f32 v250, v214 offset:64
	ds_add_f32 v250, v202 offset:96
	ds_add_f32 v250, v194 offset:256
	ds_add_f32 v250, v184 offset:288
	ds_add_f32 v250, v164 offset:320
	ds_add_f32 v250, v160 offset:352
	s_mov_b64 exec, -1
	s_waitcnt lgkmcnt(0)
	s_barrier
	s_cmp_lg_u32 s50, 0
	s_cbranch_scc1 .LBB3_27
	v_mbcnt_lo_u32_b32 v2, -1, 0
	v_mbcnt_hi_u32_b32 v2, -1, v2
	v_and_b32_e32 v3, 32, v2
	v_add_u32_e32 v4, v2, v3
	v_lshl_add_u32 v5, v4, 2, s49
	ds_read_b32 v6, v5
	v_lshl_add_u32 v4, v3, 1, v4
	v_add_u32_e32 v4, s48, v4
	v_lshlrev_b32_e32 v4, 2, v4
	s_waitcnt lgkmcnt(0)
	global_atomic_add_f32 v4, v6, s[46:47]
